# phaseA scalar branches instead of exec masks; residual loads hoisted 2kt earlier into dead regs; audio residual loads hoisted above video stores; vmcnt recomputed
# speedup vs baseline: 1.0192x; 1.0192x over previous
.LBB3_12:
	s_or_b64 exec, exec, s[10:11]
	v_or_b32_e32 v3, v51, v1
	v_lshlrev_b32_e32 v166, 6, v3
	v_or_b32_e32 v167, 0x300, v166
	v_or_b32_e32 v3, v162, v167
	v_lshlrev_b32_e32 v3, 4, v3
	v_or_b32_e32 v35, v163, v167
	v_lshlrev_b32_e32 v35, 4, v35
	global_load_dwordx4 v[114:117], v3, s[8:9]
	global_load_dwordx4 v[118:121], v35, s[8:9]
	v_or_b32_e32 v3, v164, v167
	v_lshlrev_b32_e32 v3, 4, v3
	global_load_dwordx4 v[122:125], v3, s[8:9]
	v_mul_u32_u24_e32 v3, 0x3000, v208
	v_or_b32_e32 v161, v3, v202
	v_add_u32_e32 v165, v150, v202
	ds_read_b128 v[152:155], v161
	ds_read_b128 v[146:149], v161 offset:4096
	ds_read_b128 v[142:145], v161 offset:8192
	s_waitcnt vmcnt(16)
	ds_write_b128 v165, v[126:129] offset:24576
	s_waitcnt vmcnt(15)
	ds_write_b128 v165, v[130:133] offset:32768
	s_waitcnt vmcnt(14)
	ds_write_b128 v165, v[134:137] offset:40960
	ds_read_b128 v[138:141], v161 offset:1024
	ds_read_b128 v[130:133], v161 offset:5120
	ds_read_b128 v[126:129], v161 offset:9216
	v_mov_b32_e32 v3, v50
	v_mov_b32_e32 v35, v52
	s_waitcnt lgkmcnt(8)
	v_mfma_f32_32x32x16_bf16 v[18:33], v[152:155], v[110:113], v[18:33]
	s_cmp_lg_u64 s[4:5], 0
	s_cbranch_scc0 .LBB3_14
	s_waitcnt lgkmcnt(7)
	v_mfma_f32_32x32x16_bf16 v[2:17], v[110:113], v[146:149], v[2:17]
	s_waitcnt lgkmcnt(6)
	v_mfma_f32_32x32x16_bf16 v[34:49], v[110:113], v[142:145], v[34:49]
	s_branch .LBB3_16
.LBB3_14:
	s_waitcnt lgkmcnt(7)
	v_mfma_f32_32x32x16_bf16 v[2:17], v[146:149], v[110:113], v[2:17]
	s_waitcnt lgkmcnt(6)
	v_mfma_f32_32x32x16_bf16 v[34:49], v[142:145], v[110:113], v[34:49]
.LBB3_16:
	ds_read_b128 v[134:137], v161 offset:2048
	ds_read_b128 v[110:113], v161 offset:6144
	ds_read_b128 v[50:53], v161 offset:10240
	s_waitcnt lgkmcnt(5)
	v_mfma_f32_32x32x16_bf16 v[18:33], v[138:141], v[94:97], v[18:33]
	s_cmp_lg_u64 s[4:5], 0
	s_cbranch_scc0 .LBB3_18
	s_waitcnt lgkmcnt(4)
	v_mfma_f32_32x32x16_bf16 v[2:17], v[94:97], v[130:133], v[2:17]
	s_waitcnt lgkmcnt(3)
	v_mfma_f32_32x32x16_bf16 v[34:49], v[94:97], v[126:129], v[34:49]
	s_branch .LBB3_20
.LBB3_18:
	s_waitcnt lgkmcnt(4)
	v_mfma_f32_32x32x16_bf16 v[2:17], v[130:133], v[94:97], v[2:17]
	s_waitcnt lgkmcnt(3)
	v_mfma_f32_32x32x16_bf16 v[34:49], v[126:129], v[94:97], v[34:49]
.LBB3_20:
	s_waitcnt lgkmcnt(3)
	s_barrier
	s_waitcnt lgkmcnt(4)
	ds_read_b128 v[130:133], v161 offset:3072
	s_waitcnt lgkmcnt(4)
	ds_read_b128 v[126:129], v161 offset:7168
	ds_read_b128 v[94:97], v161 offset:11264
	s_waitcnt lgkmcnt(5)
	v_mfma_f32_32x32x16_bf16 v[18:33], v[134:137], v[90:93], v[18:33]
	s_cmp_lg_u64 s[4:5], 0
	s_cbranch_scc0 .LBB3_22
	s_waitcnt lgkmcnt(4)
	v_mfma_f32_32x32x16_bf16 v[2:17], v[90:93], v[110:113], v[2:17]
	s_waitcnt lgkmcnt(3)
	v_mfma_f32_32x32x16_bf16 v[34:49], v[90:93], v[50:53], v[34:49]
	s_branch .LBB3_24
.LBB3_22:
	s_waitcnt lgkmcnt(4)
	v_mfma_f32_32x32x16_bf16 v[2:17], v[110:113], v[90:93], v[2:17]
	s_waitcnt lgkmcnt(3)
	v_mfma_f32_32x32x16_bf16 v[34:49], v[50:53], v[90:93], v[34:49]
.LBB3_24:
	ds_read_b128 v[138:141], v161 offset:28672
	ds_read_b128 v[142:145], v161 offset:24576
	ds_read_b128 v[134:137], v161 offset:32768
	s_waitcnt lgkmcnt(5)
	v_mfma_f32_32x32x16_bf16 v[18:33], v[130:133], v[86:89], v[18:33]
	s_cmp_lg_u64 s[4:5], 0
	s_cbranch_scc0 .LBB3_26
	s_waitcnt lgkmcnt(4)
	v_mfma_f32_32x32x16_bf16 v[2:17], v[86:89], v[126:129], v[2:17]
	s_waitcnt lgkmcnt(3)
	v_mfma_f32_32x32x16_bf16 v[34:49], v[86:89], v[94:97], v[34:49]
	s_branch .LBB3_28
.LBB3_26:
	s_waitcnt lgkmcnt(4)
	v_mfma_f32_32x32x16_bf16 v[2:17], v[126:129], v[86:89], v[2:17]
	s_waitcnt lgkmcnt(3)
	v_mfma_f32_32x32x16_bf16 v[34:49], v[94:97], v[86:89], v[34:49]
.LBB3_28:
	v_add_co_u32_e32 v50, vcc, 0x3000, v158
	s_nop 1
	v_addc_co_u32_e32 v51, vcc, 0, v159, vcc
	s_waitcnt lgkmcnt(3)
	global_load_dwordx4 v[94:97], v[50:51], off
	global_load_dwordx4 v[90:93], v[50:51], off offset:1024
	global_load_dwordx4 v[86:89], v[50:51], off offset:2048
	s_nop 0
	global_load_dwordx4 v[50:53], v[50:51], off offset:3072
	v_add_u32_e32 v130, 0x100, v167
	v_or_b32_e32 v110, v162, v130
	v_or_b32_e32 v111, v163, v130
	v_or_b32_e32 v130, v164, v130
	v_lshlrev_b32_e32 v110, 4, v110
	v_lshlrev_b32_e32 v126, 4, v111
	v_lshlrev_b32_e32 v130, 4, v130
	global_load_dwordx4 v[110:113], v110, s[8:9]
	s_nop 0
	global_load_dwordx4 v[126:129], v126, s[8:9]
	s_nop 0
	global_load_dwordx4 v[130:133], v130, s[8:9]
	s_waitcnt vmcnt(12)
	ds_write_b128 v165, v[98:101] offset:49152
	s_waitcnt vmcnt(11)
	ds_write_b128 v165, v[102:105] offset:57344
	v_or_b32_e32 v98, 0x10000, v150
	v_add_u32_e32 v168, v98, v202
	s_waitcnt vmcnt(10)
	ds_write_b128 v168, v[106:109]
	ds_read_b128 v[106:109], v161 offset:29696
	ds_read_b128 v[146:149], v161 offset:25600
	ds_read_b128 v[102:105], v161 offset:33792
	s_waitcnt lgkmcnt(7)
	v_mfma_f32_32x32x16_bf16 v[18:33], v[142:145], v[82:85], v[18:33]
	s_cmp_lg_u64 s[4:5], 0
	s_cbranch_scc0 .LBB3_30
	v_mfma_f32_32x32x16_bf16 v[2:17], v[82:85], v[138:141], v[2:17]
	s_waitcnt lgkmcnt(6)
	v_mfma_f32_32x32x16_bf16 v[34:49], v[82:85], v[134:137], v[34:49]
	s_branch .LBB3_32
.LBB3_30:
	v_mfma_f32_32x32x16_bf16 v[2:17], v[138:141], v[82:85], v[2:17]
	s_waitcnt lgkmcnt(6)
	v_mfma_f32_32x32x16_bf16 v[34:49], v[134:137], v[82:85], v[34:49]
.LBB3_32:
	ds_read_b128 v[98:101], v161 offset:30720
	s_waitcnt lgkmcnt(7)
	ds_read_b128 v[134:137], v161 offset:26624
	ds_read_b128 v[82:85], v161 offset:34816
	s_waitcnt lgkmcnt(4)
	v_mfma_f32_32x32x16_bf16 v[18:33], v[146:149], v[78:81], v[18:33]
	s_cmp_lg_u64 s[4:5], 0
	s_cbranch_scc0 .LBB3_34
	v_mfma_f32_32x32x16_bf16 v[2:17], v[78:81], v[106:109], v[2:17]
	s_waitcnt lgkmcnt(3)
	v_mfma_f32_32x32x16_bf16 v[34:49], v[78:81], v[102:105], v[34:49]
	s_branch .LBB3_36
.LBB3_34:
	v_mfma_f32_32x32x16_bf16 v[2:17], v[106:109], v[78:81], v[2:17]
	s_waitcnt lgkmcnt(3)
	v_mfma_f32_32x32x16_bf16 v[34:49], v[102:105], v[78:81], v[34:49]
.LBB3_36:
	s_waitcnt lgkmcnt(3)
	s_barrier
	ds_read_b128 v[106:109], v161 offset:31744
	ds_read_b128 v[138:141], v161 offset:27648
	ds_read_b128 v[78:81], v161 offset:35840
	s_waitcnt lgkmcnt(4)
	v_mfma_f32_32x32x16_bf16 v[18:33], v[134:137], v[74:77], v[18:33]
	s_cmp_lg_u64 s[4:5], 0
	s_cbranch_scc0 .LBB3_38
	v_mfma_f32_32x32x16_bf16 v[2:17], v[74:77], v[98:101], v[2:17]
	s_waitcnt lgkmcnt(3)
	v_mfma_f32_32x32x16_bf16 v[34:49], v[74:77], v[82:85], v[34:49]
	s_branch .LBB3_40
.LBB3_38:
	v_mfma_f32_32x32x16_bf16 v[2:17], v[98:101], v[74:77], v[2:17]
	s_waitcnt lgkmcnt(3)
	v_mfma_f32_32x32x16_bf16 v[34:49], v[82:85], v[74:77], v[34:49]
.LBB3_40:
	ds_read_b128 v[150:153], v161 offset:49152
	ds_read_b128 v[102:105], v161 offset:53248
	s_waitcnt lgkmcnt(5)
	ds_read_b128 v[82:85], v161 offset:57344
	s_waitcnt lgkmcnt(4)
	v_mfma_f32_32x32x16_bf16 v[18:33], v[138:141], v[70:73], v[18:33]
	s_cmp_lg_u64 s[4:5], 0
	s_cbranch_scc0 .LBB3_42
	v_mfma_f32_32x32x16_bf16 v[2:17], v[70:73], v[106:109], v[2:17]
	s_waitcnt lgkmcnt(3)
	v_mfma_f32_32x32x16_bf16 v[34:49], v[70:73], v[78:81], v[34:49]
	s_branch .LBB3_44
.LBB3_42:
	v_mfma_f32_32x32x16_bf16 v[2:17], v[106:109], v[70:73], v[2:17]
	s_waitcnt lgkmcnt(3)
	v_mfma_f32_32x32x16_bf16 v[34:49], v[78:81], v[70:73], v[34:49]
.LBB3_44:
	v_add_co_u32_e32 v70, vcc, 0x4000, v158
	s_nop 1
	v_addc_co_u32_e32 v71, vcc, 0, v159, vcc
	global_load_dwordx4 v[98:101], v[70:71], off
	s_waitcnt lgkmcnt(3)
	global_load_dwordx4 v[78:81], v[70:71], off offset:1024
	global_load_dwordx4 v[74:77], v[70:71], off offset:2048
	s_nop 0
	global_load_dwordx4 v[70:73], v[70:71], off offset:3072
	v_add_u32_e32 v138, 0x200, v167
	v_or_b32_e32 v106, v162, v138
	v_or_b32_e32 v107, v163, v138
	v_or_b32_e32 v138, v164, v138
	v_lshlrev_b32_e32 v106, 4, v106
	v_lshlrev_b32_e32 v134, 4, v107
	v_lshlrev_b32_e32 v138, 4, v138
	global_load_dwordx4 v[106:109], v106, s[8:9]
	s_nop 0
	global_load_dwordx4 v[134:137], v134, s[8:9]
	s_nop 0
	global_load_dwordx4 v[138:141], v138, s[8:9]
	ds_read_b128 v[154:157], v161 offset:50176
	ds_read_b128 v[146:149], v161 offset:54272
	ds_read_b128 v[142:145], v161 offset:58368
	s_waitcnt vmcnt(16)
	ds_write_b128 v165, v[114:117]
	s_waitcnt vmcnt(15)
	ds_write_b128 v165, v[118:121] offset:8192
	s_waitcnt vmcnt(14)
	ds_write_b128 v165, v[122:125] offset:16384
	s_waitcnt lgkmcnt(8)
	v_mfma_f32_32x32x16_bf16 v[18:33], v[150:153], v[66:69], v[18:33]
	s_cmp_lg_u64 s[4:5], 0
	s_cbranch_scc0 .LBB3_46
	s_waitcnt lgkmcnt(7)
	v_mfma_f32_32x32x16_bf16 v[2:17], v[66:69], v[102:105], v[2:17]
	s_waitcnt lgkmcnt(6)
	v_mfma_f32_32x32x16_bf16 v[34:49], v[66:69], v[82:85], v[34:49]
	s_branch .LBB3_48
.LBB3_46:
	s_waitcnt lgkmcnt(7)
	v_mfma_f32_32x32x16_bf16 v[2:17], v[102:105], v[66:69], v[2:17]
	s_waitcnt lgkmcnt(6)
	v_mfma_f32_32x32x16_bf16 v[34:49], v[82:85], v[66:69], v[34:49]
.LBB3_48:
	ds_read_b128 v[114:117], v161 offset:51200
	s_waitcnt lgkmcnt(7)
	ds_read_b128 v[82:85], v161 offset:55296
	ds_read_b128 v[66:69], v161 offset:59392
	s_waitcnt lgkmcnt(8)
	v_mfma_f32_32x32x16_bf16 v[18:33], v[154:157], v[62:65], v[18:33]
	s_cmp_lg_u64 s[4:5], 0
	s_cbranch_scc0 .LBB3_50
	s_waitcnt lgkmcnt(7)
	v_mfma_f32_32x32x16_bf16 v[2:17], v[62:65], v[146:149], v[2:17]
	s_waitcnt lgkmcnt(6)
	v_mfma_f32_32x32x16_bf16 v[34:49], v[62:65], v[142:145], v[34:49]
	s_branch .LBB3_52
.LBB3_50:
	s_waitcnt lgkmcnt(7)
	v_mfma_f32_32x32x16_bf16 v[2:17], v[146:149], v[62:65], v[2:17]
	s_waitcnt lgkmcnt(6)
	v_mfma_f32_32x32x16_bf16 v[34:49], v[142:145], v[62:65], v[34:49]
.LBB3_52:
	s_waitcnt lgkmcnt(3)
	s_barrier
	ds_read_b128 v[118:121], v161 offset:52224
	ds_read_b128 v[102:105], v161 offset:56320
	ds_read_b128 v[62:65], v161 offset:60416
	s_waitcnt lgkmcnt(5)
	v_mfma_f32_32x32x16_bf16 v[18:33], v[114:117], v[58:61], v[18:33]
	s_cmp_lg_u64 s[4:5], 0
	s_cbranch_scc0 .LBB3_54
	s_waitcnt lgkmcnt(4)
	v_mfma_f32_32x32x16_bf16 v[2:17], v[58:61], v[82:85], v[2:17]
	s_waitcnt lgkmcnt(3)
	v_mfma_f32_32x32x16_bf16 v[34:49], v[58:61], v[66:69], v[34:49]
	s_branch .LBB3_56
.LBB3_54:
	s_waitcnt lgkmcnt(4)
	v_mfma_f32_32x32x16_bf16 v[2:17], v[82:85], v[58:61], v[2:17]
	s_waitcnt lgkmcnt(3)
	v_mfma_f32_32x32x16_bf16 v[34:49], v[66:69], v[58:61], v[34:49]
.LBB3_56:
	ds_read_b128 v[142:145], v161
	s_waitcnt lgkmcnt(4)
	ds_read_b128 v[66:69], v161 offset:4096
	ds_read_b128 v[58:61], v161 offset:8192
	s_waitcnt lgkmcnt(5)
	v_mfma_f32_32x32x16_bf16 v[18:33], v[118:121], v[54:57], v[18:33]
	s_cmp_lg_u64 s[4:5], 0
	s_cbranch_scc0 .LBB3_58
	s_waitcnt lgkmcnt(4)
	v_mfma_f32_32x32x16_bf16 v[2:17], v[54:57], v[102:105], v[2:17]
	s_waitcnt lgkmcnt(3)
	v_mfma_f32_32x32x16_bf16 v[34:49], v[54:57], v[62:65], v[34:49]
	s_branch .LBB3_60
.LBB3_58:
	s_waitcnt lgkmcnt(4)
	v_mfma_f32_32x32x16_bf16 v[2:17], v[102:105], v[54:57], v[2:17]
	s_waitcnt lgkmcnt(3)
	v_mfma_f32_32x32x16_bf16 v[34:49], v[62:65], v[54:57], v[34:49]
.LBB3_60:
	v_add_co_u32_e32 v54, vcc, 0x5000, v158
	s_nop 1
	v_addc_co_u32_e32 v55, vcc, 0, v159, vcc
	s_waitcnt lgkmcnt(4)
	global_load_dwordx4 v[102:105], v[54:55], off
	global_load_dwordx4 v[82:85], v[54:55], off offset:1024
	s_waitcnt lgkmcnt(3)
	global_load_dwordx4 v[62:65], v[54:55], off offset:2048
	s_nop 0
	global_load_dwordx4 v[54:57], v[54:55], off offset:3072
	v_add_u32_e32 v122, 0x300, v167
	v_or_b32_e32 v114, v162, v122
	v_or_b32_e32 v115, v163, v122
	v_or_b32_e32 v122, v164, v122
	v_lshlrev_b32_e32 v114, 4, v114
	v_lshlrev_b32_e32 v118, 4, v115
	v_lshlrev_b32_e32 v122, 4, v122
	global_load_dwordx4 v[114:117], v114, s[8:9]
	s_nop 0
	global_load_dwordx4 v[118:121], v118, s[8:9]
	s_nop 0
	global_load_dwordx4 v[122:125], v122, s[8:9]
	s_waitcnt vmcnt(16)
	ds_write_b128 v165, v[110:113] offset:24576
	s_waitcnt vmcnt(15)
	ds_write_b128 v165, v[126:129] offset:32768
	s_waitcnt vmcnt(14)
	ds_write_b128 v165, v[130:133] offset:40960
	ds_read_b128 v[146:149], v161 offset:1024
	ds_read_b128 v[126:129], v161 offset:5120
	ds_read_b128 v[110:113], v161 offset:9216
	s_waitcnt lgkmcnt(8)
	v_mfma_f32_32x32x16_bf16 v[18:33], v[142:145], v[94:97], v[18:33]
	s_cmp_lg_u64 s[4:5], 0
	s_cbranch_scc0 .LBB3_62
	s_waitcnt lgkmcnt(7)
	v_mfma_f32_32x32x16_bf16 v[2:17], v[94:97], v[66:69], v[2:17]
	s_waitcnt lgkmcnt(6)
	v_mfma_f32_32x32x16_bf16 v[34:49], v[94:97], v[58:61], v[34:49]
	s_branch .LBB3_64
.LBB3_62:
	s_waitcnt lgkmcnt(7)
	v_mfma_f32_32x32x16_bf16 v[2:17], v[66:69], v[94:97], v[2:17]
	s_waitcnt lgkmcnt(6)
	v_mfma_f32_32x32x16_bf16 v[34:49], v[58:61], v[94:97], v[34:49]
.LBB3_64:
	ds_read_b128 v[130:133], v161 offset:2048
	ds_read_b128 v[94:97], v161 offset:6144
	s_waitcnt lgkmcnt(8)
	ds_read_b128 v[58:61], v161 offset:10240
	s_waitcnt lgkmcnt(5)
	v_mfma_f32_32x32x16_bf16 v[18:33], v[146:149], v[90:93], v[18:33]
	s_cmp_lg_u64 s[4:5], 0
	s_cbranch_scc0 .LBB3_66
	s_waitcnt lgkmcnt(4)
	v_mfma_f32_32x32x16_bf16 v[2:17], v[90:93], v[126:129], v[2:17]
	s_waitcnt lgkmcnt(3)
	v_mfma_f32_32x32x16_bf16 v[34:49], v[90:93], v[110:113], v[34:49]
	s_branch .LBB3_68
.LBB3_66:
	s_waitcnt lgkmcnt(4)
	v_mfma_f32_32x32x16_bf16 v[2:17], v[126:129], v[90:93], v[2:17]
	s_waitcnt lgkmcnt(3)
	v_mfma_f32_32x32x16_bf16 v[34:49], v[110:113], v[90:93], v[34:49]
.LBB3_68:
	s_waitcnt lgkmcnt(3)
	s_barrier
	s_waitcnt lgkmcnt(3)
	ds_read_b128 v[110:113], v161 offset:3072
	ds_read_b128 v[90:93], v161 offset:7168
	ds_read_b128 v[66:69], v161 offset:11264
	s_waitcnt lgkmcnt(5)
	v_mfma_f32_32x32x16_bf16 v[18:33], v[130:133], v[86:89], v[18:33]
	s_cmp_lg_u64 s[4:5], 0
	s_cbranch_scc0 .LBB3_70
	s_waitcnt lgkmcnt(4)
	v_mfma_f32_32x32x16_bf16 v[2:17], v[86:89], v[94:97], v[2:17]
	s_waitcnt lgkmcnt(3)
	v_mfma_f32_32x32x16_bf16 v[34:49], v[86:89], v[58:61], v[34:49]
	s_branch .LBB3_72
.LBB3_70:
	s_waitcnt lgkmcnt(4)
	v_mfma_f32_32x32x16_bf16 v[2:17], v[94:97], v[86:89], v[2:17]
	s_waitcnt lgkmcnt(3)
	v_mfma_f32_32x32x16_bf16 v[34:49], v[58:61], v[86:89], v[34:49]
.LBB3_72:
	ds_read_b128 v[130:133], v161 offset:28672
	ds_read_b128 v[142:145], v161 offset:24576
	s_waitcnt lgkmcnt(5)
	ds_read_b128 v[58:61], v161 offset:32768
	s_waitcnt lgkmcnt(5)
	v_mfma_f32_32x32x16_bf16 v[18:33], v[110:113], v[50:53], v[18:33]
	s_cmp_lg_u64 s[4:5], 0
	s_cbranch_scc0 .LBB3_74
	s_waitcnt lgkmcnt(4)
	v_mfma_f32_32x32x16_bf16 v[2:17], v[50:53], v[90:93], v[2:17]
	s_waitcnt lgkmcnt(3)
	v_mfma_f32_32x32x16_bf16 v[34:49], v[50:53], v[66:69], v[34:49]
	s_branch .LBB3_76
.LBB3_74:
	s_waitcnt lgkmcnt(4)
	v_mfma_f32_32x32x16_bf16 v[2:17], v[90:93], v[50:53], v[2:17]
	s_waitcnt lgkmcnt(3)
	v_mfma_f32_32x32x16_bf16 v[34:49], v[66:69], v[50:53], v[34:49]
.LBB3_76:
	v_add_co_u32_e32 v50, vcc, 0x6000, v158
	s_nop 1
	v_addc_co_u32_e32 v51, vcc, 0, v159, vcc
	s_waitcnt lgkmcnt(4)
	global_load_dwordx4 v[90:93], v[50:51], off
	global_load_dwordx4 v[86:89], v[50:51], off offset:1024
	s_waitcnt lgkmcnt(3)
	global_load_dwordx4 v[66:69], v[50:51], off offset:2048
	s_nop 0
	global_load_dwordx4 v[50:53], v[50:51], off offset:3072
	v_or_b32_e32 v126, 0x700, v166
	v_or_b32_e32 v94, v162, v126
	v_or_b32_e32 v95, v163, v126
	v_or_b32_e32 v126, v164, v126
	v_lshlrev_b32_e32 v94, 4, v94
	v_lshlrev_b32_e32 v110, 4, v95
	v_lshlrev_b32_e32 v126, 4, v126
	global_load_dwordx4 v[94:97], v94, s[8:9]
	s_nop 0
	global_load_dwordx4 v[110:113], v110, s[8:9]
	s_nop 0
	global_load_dwordx4 v[126:129], v126, s[8:9]
	s_waitcnt vmcnt(16)
	ds_write_b128 v165, v[106:109] offset:49152
	s_waitcnt vmcnt(15)
	ds_write_b128 v165, v[134:137] offset:57344
	s_waitcnt vmcnt(14)
	ds_write_b128 v168, v[138:141]
	ds_read_b128 v[134:137], v161 offset:29696
	ds_read_b128 v[146:149], v161 offset:25600
	ds_read_b128 v[106:109], v161 offset:33792
	s_waitcnt lgkmcnt(7)
	v_mfma_f32_32x32x16_bf16 v[18:33], v[142:145], v[98:101], v[18:33]
	s_cmp_lg_u64 s[4:5], 0
	s_cbranch_scc0 .LBB3_78
	v_mfma_f32_32x32x16_bf16 v[2:17], v[98:101], v[130:133], v[2:17]
	s_waitcnt lgkmcnt(6)
	v_mfma_f32_32x32x16_bf16 v[34:49], v[98:101], v[58:61], v[34:49]
	s_branch .LBB3_80
.LBB3_78:
	v_mfma_f32_32x32x16_bf16 v[2:17], v[130:133], v[98:101], v[2:17]
	s_waitcnt lgkmcnt(6)
	v_mfma_f32_32x32x16_bf16 v[34:49], v[58:61], v[98:101], v[34:49]
.LBB3_80:
	ds_read_b128 v[98:101], v161 offset:30720
	ds_read_b128 v[138:141], v161 offset:26624
	s_waitcnt lgkmcnt(8)
	ds_read_b128 v[58:61], v161 offset:34816
	s_waitcnt lgkmcnt(4)
	v_mfma_f32_32x32x16_bf16 v[18:33], v[146:149], v[78:81], v[18:33]
	s_cmp_lg_u64 s[4:5], 0
	s_cbranch_scc0 .LBB3_82
	v_mfma_f32_32x32x16_bf16 v[2:17], v[78:81], v[134:137], v[2:17]
	s_waitcnt lgkmcnt(3)
	v_mfma_f32_32x32x16_bf16 v[34:49], v[78:81], v[106:109], v[34:49]
	s_branch .LBB3_84
.LBB3_82:
	v_mfma_f32_32x32x16_bf16 v[2:17], v[134:137], v[78:81], v[2:17]
	s_waitcnt lgkmcnt(3)
	v_mfma_f32_32x32x16_bf16 v[34:49], v[106:109], v[78:81], v[34:49]
.LBB3_84:
	s_waitcnt lgkmcnt(3)
	s_barrier
	ds_read_b128 v[130:133], v161 offset:31744
	ds_read_b128 v[134:137], v161 offset:27648
	ds_read_b128 v[78:81], v161 offset:35840
	s_waitcnt lgkmcnt(4)
	v_mfma_f32_32x32x16_bf16 v[18:33], v[138:141], v[74:77], v[18:33]
	s_cmp_lg_u64 s[4:5], 0
	s_cbranch_scc0 .LBB3_86
	v_mfma_f32_32x32x16_bf16 v[2:17], v[74:77], v[98:101], v[2:17]
	s_waitcnt lgkmcnt(3)
	v_mfma_f32_32x32x16_bf16 v[34:49], v[74:77], v[58:61], v[34:49]
	s_branch .LBB3_88
.LBB3_86:
	v_mfma_f32_32x32x16_bf16 v[2:17], v[98:101], v[74:77], v[2:17]
	s_waitcnt lgkmcnt(3)
	v_mfma_f32_32x32x16_bf16 v[34:49], v[58:61], v[74:77], v[34:49]
.LBB3_88:
	ds_read_b128 v[138:141], v161 offset:49152
	ds_read_b128 v[106:109], v161 offset:53248
	ds_read_b128 v[98:101], v161 offset:57344
	s_waitcnt lgkmcnt(4)
	v_mfma_f32_32x32x16_bf16 v[18:33], v[134:137], v[70:73], v[18:33]
	s_cmp_lg_u64 s[4:5], 0
	s_cbranch_scc0 .LBB3_90
	v_mfma_f32_32x32x16_bf16 v[2:17], v[70:73], v[130:133], v[2:17]
	s_waitcnt lgkmcnt(3)
	v_mfma_f32_32x32x16_bf16 v[34:49], v[70:73], v[78:81], v[34:49]
	s_branch .LBB3_92
.LBB3_90:
	v_mfma_f32_32x32x16_bf16 v[2:17], v[130:133], v[70:73], v[2:17]
	s_waitcnt lgkmcnt(3)
	v_mfma_f32_32x32x16_bf16 v[34:49], v[78:81], v[70:73], v[34:49]
.LBB3_92:
	v_add_co_u32_e32 v58, vcc, 0x7000, v158
	s_nop 1
	v_addc_co_u32_e32 v59, vcc, 0, v159, vcc
	s_waitcnt lgkmcnt(3)
	global_load_dwordx4 v[78:81], v[58:59], off
	global_load_dwordx4 v[74:77], v[58:59], off offset:1024
	global_load_dwordx4 v[70:73], v[58:59], off offset:2048
	s_nop 0
	global_load_dwordx4 v[58:61], v[58:59], off offset:3072
	ds_read_b128 v[142:145], v161 offset:50176
	ds_read_b128 v[134:137], v161 offset:54272
	ds_read_b128 v[130:133], v161 offset:58368
	s_waitcnt vmcnt(13)
	ds_write_b128 v165, v[114:117]
	s_waitcnt vmcnt(12)
	ds_write_b128 v165, v[118:121] offset:8192
	s_waitcnt vmcnt(11)
	ds_write_b128 v165, v[122:125] offset:16384
	s_waitcnt lgkmcnt(8)
	v_mfma_f32_32x32x16_bf16 v[18:33], v[138:141], v[102:105], v[18:33]
	s_cmp_lg_u64 s[4:5], 0
	s_cbranch_scc0 .LBB3_94
	s_waitcnt lgkmcnt(7)
	v_mfma_f32_32x32x16_bf16 v[2:17], v[102:105], v[106:109], v[2:17]
	s_waitcnt lgkmcnt(6)
	v_mfma_f32_32x32x16_bf16 v[34:49], v[102:105], v[98:101], v[34:49]
	s_branch .LBB3_96
.LBB3_94:
	s_waitcnt lgkmcnt(7)
	v_mfma_f32_32x32x16_bf16 v[2:17], v[106:109], v[102:105], v[2:17]
	s_waitcnt lgkmcnt(6)
	v_mfma_f32_32x32x16_bf16 v[34:49], v[98:101], v[102:105], v[34:49]
.LBB3_96:
	ds_read_b128 v[114:117], v161 offset:51200
	ds_read_b128 v[102:105], v161 offset:55296
	s_waitcnt lgkmcnt(8)
	ds_read_b128 v[98:101], v161 offset:59392
	s_waitcnt lgkmcnt(8)
	v_mfma_f32_32x32x16_bf16 v[18:33], v[142:145], v[82:85], v[18:33]
	s_cmp_lg_u64 s[4:5], 0
	s_cbranch_scc0 .LBB3_98
	s_waitcnt lgkmcnt(7)
	v_mfma_f32_32x32x16_bf16 v[2:17], v[82:85], v[134:137], v[2:17]
	s_waitcnt lgkmcnt(6)
	v_mfma_f32_32x32x16_bf16 v[34:49], v[82:85], v[130:133], v[34:49]
	s_branch .LBB3_100
.LBB3_98:
	s_waitcnt lgkmcnt(7)
	v_mfma_f32_32x32x16_bf16 v[2:17], v[134:137], v[82:85], v[2:17]
	s_waitcnt lgkmcnt(6)
	v_mfma_f32_32x32x16_bf16 v[34:49], v[130:133], v[82:85], v[34:49]
.LBB3_100:
	s_waitcnt lgkmcnt(3)
	s_barrier
	ds_read_b128 v[118:121], v161 offset:52224
	ds_read_b128 v[106:109], v161 offset:56320
	ds_read_b128 v[82:85], v161 offset:60416
	s_waitcnt lgkmcnt(5)
	v_mfma_f32_32x32x16_bf16 v[18:33], v[114:117], v[62:65], v[18:33]
	s_cmp_lg_u64 s[4:5], 0
	s_cbranch_scc0 .LBB3_102
	s_waitcnt lgkmcnt(4)
	v_mfma_f32_32x32x16_bf16 v[2:17], v[62:65], v[102:105], v[2:17]
	s_waitcnt lgkmcnt(3)
	v_mfma_f32_32x32x16_bf16 v[34:49], v[62:65], v[98:101], v[34:49]
	s_branch .LBB3_104
.LBB3_102:
	s_waitcnt lgkmcnt(4)
	v_mfma_f32_32x32x16_bf16 v[2:17], v[102:105], v[62:65], v[2:17]
	s_waitcnt lgkmcnt(3)
	v_mfma_f32_32x32x16_bf16 v[34:49], v[98:101], v[62:65], v[34:49]
.LBB3_104:
	s_waitcnt lgkmcnt(4)
	ds_read_b128 v[102:105], v161
	s_waitcnt lgkmcnt(4)
	ds_read_b128 v[98:101], v161 offset:4096
	ds_read_b128 v[62:65], v161 offset:8192
	s_waitcnt lgkmcnt(5)
	v_mfma_f32_32x32x16_bf16 v[18:33], v[118:121], v[54:57], v[18:33]
	s_cmp_lg_u64 s[4:5], 0
	s_cbranch_scc0 .LBB3_106
	s_waitcnt lgkmcnt(4)
	v_mfma_f32_32x32x16_bf16 v[2:17], v[54:57], v[106:109], v[2:17]
	s_waitcnt lgkmcnt(3)
	v_mfma_f32_32x32x16_bf16 v[34:49], v[54:57], v[82:85], v[34:49]
	s_branch .LBB3_108
.LBB3_106:
	s_waitcnt lgkmcnt(4)
	v_mfma_f32_32x32x16_bf16 v[2:17], v[106:109], v[54:57], v[2:17]
	s_waitcnt lgkmcnt(3)
	v_mfma_f32_32x32x16_bf16 v[34:49], v[82:85], v[54:57], v[34:49]
.LBB3_108:
	s_waitcnt vmcnt(6)
	ds_write_b128 v165, v[94:97] offset:24576
	s_waitcnt vmcnt(5)
	ds_write_b128 v165, v[110:113] offset:32768
	s_waitcnt vmcnt(4)
	ds_write_b128 v165, v[126:129] offset:40960
	s_waitcnt lgkmcnt(7)
	ds_read_b128 v[106:109], v161 offset:1024
	ds_read_b128 v[94:97], v161 offset:5120
	s_waitcnt lgkmcnt(8)
	ds_read_b128 v[82:85], v161 offset:9216
	s_waitcnt lgkmcnt(8)
	v_mfma_f32_32x32x16_bf16 v[18:33], v[102:105], v[90:93], v[18:33]
	s_cmp_lg_u64 s[4:5], 0
	s_cbranch_scc0 .LBB3_110
	s_waitcnt lgkmcnt(7)
	v_mfma_f32_32x32x16_bf16 v[2:17], v[90:93], v[98:101], v[2:17]
	s_waitcnt lgkmcnt(6)
	v_mfma_f32_32x32x16_bf16 v[34:49], v[90:93], v[62:65], v[34:49]
	s_branch .LBB3_112
.LBB3_110:
	s_waitcnt lgkmcnt(7)
	v_mfma_f32_32x32x16_bf16 v[2:17], v[98:101], v[90:93], v[2:17]
	s_waitcnt lgkmcnt(6)
	v_mfma_f32_32x32x16_bf16 v[34:49], v[62:65], v[90:93], v[34:49]
.LBB3_112:
	s_waitcnt lgkmcnt(7)
	ds_read_b128 v[98:101], v161 offset:2048
	ds_read_b128 v[90:93], v161 offset:6144
	ds_read_b128 v[54:57], v161 offset:10240
	s_waitcnt lgkmcnt(5)
	v_mfma_f32_32x32x16_bf16 v[18:33], v[106:109], v[86:89], v[18:33]
	s_cmp_lg_u64 s[4:5], 0
	s_cbranch_scc0 .LBB3_114
	s_waitcnt lgkmcnt(4)
	v_mfma_f32_32x32x16_bf16 v[2:17], v[86:89], v[94:97], v[2:17]
	s_waitcnt lgkmcnt(3)
	v_mfma_f32_32x32x16_bf16 v[34:49], v[86:89], v[82:85], v[34:49]
	s_branch .LBB3_116
.LBB3_114:
	s_waitcnt lgkmcnt(4)
	v_mfma_f32_32x32x16_bf16 v[2:17], v[94:97], v[86:89], v[2:17]
	s_waitcnt lgkmcnt(3)
	v_mfma_f32_32x32x16_bf16 v[34:49], v[82:85], v[86:89], v[34:49]
.LBB3_116:
	s_waitcnt lgkmcnt(3)
	s_barrier
	ds_read_b128 v[86:89], v161 offset:3072
	s_waitcnt lgkmcnt(4)
	ds_read_b128 v[82:85], v161 offset:7168
	ds_read_b128 v[62:65], v161 offset:11264
	s_waitcnt lgkmcnt(5)
	v_mfma_f32_32x32x16_bf16 v[18:33], v[98:101], v[66:69], v[18:33]
	s_cmp_lg_u64 s[4:5], 0
	s_cbranch_scc0 .LBB3_118
	s_waitcnt lgkmcnt(4)
	v_mfma_f32_32x32x16_bf16 v[2:17], v[66:69], v[90:93], v[2:17]
	s_waitcnt lgkmcnt(3)
	v_mfma_f32_32x32x16_bf16 v[34:49], v[66:69], v[54:57], v[34:49]
	s_branch .LBB3_120
.LBB3_118:
	s_waitcnt lgkmcnt(4)
	v_mfma_f32_32x32x16_bf16 v[2:17], v[90:93], v[66:69], v[2:17]
	s_waitcnt lgkmcnt(3)
	v_mfma_f32_32x32x16_bf16 v[34:49], v[54:57], v[66:69], v[34:49]
.LBB3_120:
	ds_read_b128 v[66:69], v161 offset:28672
	s_waitcnt lgkmcnt(5)
	ds_read_b128 v[90:93], v161 offset:24576
	s_waitcnt lgkmcnt(5)
	ds_read_b128 v[54:57], v161 offset:32768
	s_waitcnt lgkmcnt(5)
	v_mfma_f32_32x32x16_bf16 v[18:33], v[86:89], v[50:53], v[18:33]
	s_cmp_lg_u64 s[4:5], 0
	s_cbranch_scc0 .LBB3_122
	s_waitcnt lgkmcnt(4)
	v_mfma_f32_32x32x16_bf16 v[2:17], v[50:53], v[82:85], v[2:17]
	s_waitcnt lgkmcnt(3)
	v_mfma_f32_32x32x16_bf16 v[34:49], v[50:53], v[62:65], v[34:49]
	s_branch .LBB3_124
.LBB3_122:
	s_waitcnt lgkmcnt(4)
	v_mfma_f32_32x32x16_bf16 v[2:17], v[82:85], v[50:53], v[2:17]
	s_waitcnt lgkmcnt(3)
	v_mfma_f32_32x32x16_bf16 v[34:49], v[62:65], v[50:53], v[34:49]
.LBB3_124:
	s_waitcnt lgkmcnt(4)
	ds_read_b128 v[82:85], v161 offset:29696
	ds_read_b128 v[86:89], v161 offset:25600
	s_waitcnt lgkmcnt(5)
	ds_read_b128 v[62:65], v161 offset:33792
	s_waitcnt vmcnt(3) lgkmcnt(4)
	v_mfma_f32_32x32x16_bf16 v[18:33], v[90:93], v[78:81], v[18:33]
	s_cmp_lg_u64 s[4:5], 0
	s_cbranch_scc0 .LBB3_126
	v_mfma_f32_32x32x16_bf16 v[2:17], v[78:81], v[66:69], v[2:17]
	s_waitcnt lgkmcnt(3)
	v_mfma_f32_32x32x16_bf16 v[34:49], v[78:81], v[54:57], v[34:49]
	s_branch .LBB3_128
.LBB3_126:
	v_mfma_f32_32x32x16_bf16 v[2:17], v[66:69], v[78:81], v[2:17]
	s_waitcnt lgkmcnt(3)
	v_mfma_f32_32x32x16_bf16 v[34:49], v[54:57], v[78:81], v[34:49]
.LBB3_128:
	s_waitcnt lgkmcnt(3)
	ds_read_b128 v[54:57], v161 offset:30720
	ds_read_b128 v[78:81], v161 offset:26624
	ds_read_b128 v[50:53], v161 offset:34816
	s_waitcnt vmcnt(2) lgkmcnt(4)
	v_mfma_f32_32x32x16_bf16 v[18:33], v[86:89], v[74:77], v[18:33]
	s_cmp_lg_u64 s[4:5], 0
	s_cbranch_scc0 .LBB3_130
	v_mfma_f32_32x32x16_bf16 v[2:17], v[74:77], v[82:85], v[2:17]
	s_waitcnt lgkmcnt(3)
	v_mfma_f32_32x32x16_bf16 v[34:49], v[74:77], v[62:65], v[34:49]
	s_branch .LBB3_132
.LBB3_130:
	v_mfma_f32_32x32x16_bf16 v[2:17], v[82:85], v[74:77], v[2:17]
	s_waitcnt lgkmcnt(3)
	v_mfma_f32_32x32x16_bf16 v[34:49], v[62:65], v[74:77], v[34:49]
.LBB3_132:
	s_waitcnt lgkmcnt(3)
	s_barrier
	ds_read_b128 v[66:69], v161 offset:31744
	ds_read_b128 v[74:77], v161 offset:27648
	s_waitcnt lgkmcnt(5)
	ds_read_b128 v[62:65], v161 offset:35840
	s_waitcnt vmcnt(1) lgkmcnt(4)
	v_mfma_f32_32x32x16_bf16 v[18:33], v[78:81], v[70:73], v[18:33]
	s_cmp_lg_u64 s[4:5], 0
	s_cbranch_scc0 .LBB3_134
	v_mfma_f32_32x32x16_bf16 v[2:17], v[70:73], v[54:57], v[2:17]
	s_waitcnt lgkmcnt(3)
	v_mfma_f32_32x32x16_bf16 v[34:49], v[70:73], v[50:53], v[34:49]
	s_branch .LBB3_136
.LBB3_134:
	v_mfma_f32_32x32x16_bf16 v[2:17], v[54:57], v[70:73], v[2:17]
	s_waitcnt lgkmcnt(3)
	v_mfma_f32_32x32x16_bf16 v[34:49], v[50:53], v[70:73], v[34:49]
.LBB3_136:
	s_load_dwordx2 s[8:9], s[0:1], 0x20
	s_waitcnt vmcnt(0) lgkmcnt(0)
	s_nop 1
	v_mfma_f32_32x32x16_bf16 v[18:33], v[74:77], v[58:61], v[18:33]
	s_cmp_lg_u64 s[4:5], 0
	s_cbranch_scc0 .LBB3_138
	v_mfma_f32_32x32x16_bf16 v[2:17], v[58:61], v[66:69], v[2:17]
	v_mfma_f32_32x32x16_bf16 v[34:49], v[58:61], v[62:65], v[34:49]
	s_branch .LBB3_140
.LBB3_138:
	v_mfma_f32_32x32x16_bf16 v[2:17], v[66:69], v[58:61], v[2:17]
	v_mfma_f32_32x32x16_bf16 v[34:49], v[62:65], v[58:61], v[34:49]
.LBB3_140:
	s_load_dwordx2 s[4:5], s[0:1], 0x30
	s_load_dwordx2 s[10:11], s[0:1], 0x0
	s_load_dwordx2 s[12:13], s[0:1], 0x28
	s_load_dwordx2 s[14:15], s[0:1], 0x38
	s_lshr_b32 s0, s2, 6
	s_add_i32 s0, s17, s0
	v_lshl_or_b32 v206, s0, 3, v1
	s_mul_i32 s0, s16, 0x180000
	v_mov_b32_e32 v207, 0
	s_add_u32 s0, s6, s0
	v_lshlrev_b32_e64 v58, 6, s23
	v_mov_b32_e32 v203, v207
	s_addc_u32 s1, s7, 0
	v_or_b32_e32 v54, v58, v160
	v_lshlrev_b32_e64 v59, 6, s3
	v_lshlrev_b64 v[50:51], 15, v[206:207]
	v_lshl_add_u64 v[52:53], s[0:1], 0, v[202:203]
	v_lshlrev_b32_e32 v206, 10, v54
	v_or_b32_e32 v56, v59, v160
	v_lshl_add_u64 v[54:55], v[52:53], 0, v[206:207]
	v_lshlrev_b32_e32 v206, 10, v56
	v_or_b32_e32 v60, 0x400, v58
	s_waitcnt lgkmcnt(0)
	s_barrier
	v_lshl_add_u64 v[56:57], v[52:53], 0, v[206:207]
	global_load_dwordx4 v[190:193], v[54:55], off
	global_load_dwordx4 v[194:197], v[56:57], off
	v_or_b32_e32 v54, v60, v160
	v_or_b32_e32 v61, 4, v160
	v_lshlrev_b32_e32 v206, 10, v54
	v_or_b32_e32 v56, v61, v58
	v_lshl_add_u64 v[54:55], v[52:53], 0, v[206:207]
	v_lshlrev_b32_e32 v206, 10, v56
	v_lshl_add_u64 v[56:57], v[52:53], 0, v[206:207]
	global_load_dwordx4 v[198:201], v[54:55], off
	global_load_dwordx4 v[174:177], v[56:57], off
	v_or_b32_e32 v54, v59, v61
	v_lshlrev_b32_e32 v206, 10, v54
	v_or_b32_e32 v56, v60, v61
	v_lshl_add_u64 v[50:51], s[10:11], 0, v[50:51]
	v_lshl_add_u64 v[54:55], v[52:53], 0, v[206:207]
	v_lshlrev_b32_e32 v206, 10, v56
	v_lshl_add_u64 v[50:51], v[50:51], 0, v[202:203]
	v_lshl_add_u64 v[52:53], v[52:53], 0, v[206:207]
	s_movk_i32 s2, 0x1000
	global_load_dwordx4 v[182:185], v[54:55], off
	global_load_dwordx4 v[186:189], v[52:53], off
	global_load_dwordx4 v[170:173], v[50:51], off
	global_load_dwordx4 v[162:165], v[50:51], off offset:1024
	global_load_dwordx4 v[154:157], v[50:51], off offset:2048
	global_load_dwordx4 v[146:149], v[50:51], off offset:3072
	v_add_co_u32_e32 v52, vcc, s2, v50
	s_movk_i32 s26, 0x2000
	s_nop 0
	v_addc_co_u32_e32 v53, vcc, 0, v51, vcc
	v_add_co_u32_e32 v50, vcc, s26, v50
	v_lshlrev_b32_e32 v1, 1, v1
	s_nop 0
	v_addc_co_u32_e32 v51, vcc, 0, v51, vcc
	global_load_dwordx4 v[166:169], v[52:53], off offset:1024
	global_load_dwordx4 v[158:161], v[52:53], off offset:2048
	global_load_dwordx4 v[178:181], v[50:51], off offset:-4096
	global_load_dwordx4 v[150:153], v[52:53], off offset:3072
	global_load_dwordx4 v[142:145], v[50:51], off
	global_load_dwordx4 v[138:141], v[50:51], off offset:1024
	global_load_dwordx4 v[134:137], v[50:51], off offset:2048
	global_load_dwordx4 v[130:133], v[50:51], off offset:3072
	v_mul_u32_u24_e32 v50, 0x6000, v205
	v_mul_u32_u24_e32 v52, 12, v208
	v_or_b32_e32 v50, v50, v202
	v_lshlrev_b32_e32 v51, 2, v204
	v_and_b32_e32 v52, 8, v52
	v_and_b32_e32 v1, 2, v1
	v_add_u32_e32 v50, 0x12000, v50
	v_or3_b32 v1, v1, v52, v51
	v_cvt_pk_bf16_f32 v18, v18, v19
	v_cvt_pk_bf16_f32 v19, v20, v21
	v_cvt_pk_bf16_f32 v20, v22, v23
	v_cvt_pk_bf16_f32 v21, v24, v25
	v_lshl_add_u32 v1, v1, 10, v50
	ds_write_b128 v1, v[18:21]
	v_cvt_pk_bf16_f32 v18, v26, v27
	v_cvt_pk_bf16_f32 v19, v28, v29
	v_cvt_pk_bf16_f32 v20, v30, v31
	v_cvt_pk_bf16_f32 v21, v32, v33
	ds_write_b128 v1, v[18:21] offset:1024
	v_mad_u32_u24 v1, v208, 3, 1
	v_lshlrev_b32_e32 v18, 2, v1
	v_lshlrev_b32_e32 v1, 1, v1
	v_and_b32_e32 v18, 24, v18
	v_and_b32_e32 v1, 2, v1
	v_or3_b32 v1, v1, v18, v51
	v_cvt_pk_bf16_f32 v2, v2, v3
	v_cvt_pk_bf16_f32 v3, v4, v5
	v_cvt_pk_bf16_f32 v4, v6, v7
	v_cvt_pk_bf16_f32 v5, v8, v9
	v_lshl_add_u32 v1, v1, 10, v50
	ds_write_b128 v1, v[2:5]
	v_cvt_pk_bf16_f32 v2, v10, v11
	v_cvt_pk_bf16_f32 v3, v12, v13
	v_cvt_pk_bf16_f32 v4, v14, v15
	v_cvt_pk_bf16_f32 v5, v16, v17
	ds_write_b128 v1, v[2:5] offset:1024
	v_mad_u32_u24 v1, v208, 3, 2
	v_lshlrev_b32_e32 v2, 2, v1
	v_lshlrev_b32_e32 v1, 1, v1
	s_lshl_b32 s2, s17, 3
	v_and_b32_e32 v2, 24, v2
	v_and_b32_e32 v1, 2, v1
	s_add_i32 s2, s22, s2
	v_or3_b32 v1, v1, v2, v51
	s_add_i32 s2, s2, 32
	v_cvt_pk_bf16_f32 v2, v34, v35
	v_cvt_pk_bf16_f32 v3, v36, v37
	v_cvt_pk_bf16_f32 v4, v38, v39
	v_cvt_pk_bf16_f32 v5, v40, v41
	v_lshl_add_u32 v1, v1, 10, v50
	s_mov_b32 s3, 0
	s_lshl_b32 s6, s23, 6
	s_and_b32 s28, s2, 0x7ffffff8
	s_lshl_b32 s2, s16, 9
	s_movk_i32 s27, 0x6000
	ds_write_b128 v1, v[2:5]
	v_cvt_pk_bf16_f32 v2, v42, v43
	v_cvt_pk_bf16_f32 v3, v44, v45
	v_cvt_pk_bf16_f32 v4, v46, v47
	v_cvt_pk_bf16_f32 v5, v48, v49
	s_mov_b32 s7, s3
	s_or_b32 s16, s2, s6
	s_mov_b32 s17, s3
	s_mov_b64 s[20:21], -1
	s_movk_i32 s29, 0x3000
	s_movk_i32 s30, 0x4000
	s_movk_i32 s31, 0x5000
	s_movk_i32 s33, 0x7000
	s_mov_b32 s34, 0x8000
	s_mov_b32 s35, 0xa000
	s_mov_b32 s36, 0xc000
	s_mov_b32 s37, 0xe000
	s_mov_b32 s38, 0xf149f2ca
	s_mov_b32 s39, 0x9000
	s_mov_b32 s40, 0xb000
	s_mov_b32 s41, 0
	ds_write_b128 v1, v[2:5] offset:1024
	s_branch .LBB3_142
.LBB3_141:
	s_mul_i32 s2, s41, 0x6000
	v_or_b32_e32 v98, s2, v206
	v_add_u32_e32 v250, 0x12000, v98
	ds_read_b128 v[98:101], v250 offset:8192
	v_cvt_pk_bf16_f32 v50, v50, v51
	v_cvt_pk_bf16_f32 v51, v52, v53
	v_cvt_pk_bf16_f32 v52, v54, v55
	v_cvt_pk_bf16_f32 v53, v56, v57
	ds_read_b128 v[54:57], v250 offset:9216
	v_cvt_pk_bf16_f32 v214, v82, v83
	v_cvt_pk_bf16_f32 v215, v84, v85
	ds_read_b128 v[82:85], v250 offset:13312
	s_waitcnt lgkmcnt(2)
	v_mfma_f32_32x32x16_bf16 v[114:129], v[98:101], v[50:53], 0
	ds_read_b128 v[98:101], v250 offset:12288
	v_cvt_pk_bf16_f32 v18, v18, v19
	v_cvt_pk_bf16_f32 v19, v20, v21
	v_cvt_pk_bf16_f32 v20, v22, v23
	v_cvt_pk_bf16_f32 v21, v24, v25
	v_cvt_pk_bf16_f32 v216, v86, v87
	v_cvt_pk_bf16_f32 v217, v88, v89
	v_cvt_pk_bf16_f32 v86, v10, v11
	s_waitcnt lgkmcnt(0)
	v_mfma_f32_32x32x16_bf16 v[98:113], v[98:101], v[50:53], 0
	v_cvt_pk_bf16_f32 v50, v58, v59
	v_cvt_pk_bf16_f32 v51, v60, v61
	v_cvt_pk_bf16_f32 v52, v62, v63
	v_cvt_pk_bf16_f32 v53, v64, v65
	ds_read_b128 v[58:61], v250 offset:10240
	v_cvt_pk_bf16_f32 v87, v12, v13
	v_cvt_pk_bf16_f32 v88, v14, v15
	v_mfma_f32_32x32x16_bf16 v[114:129], v[54:57], v[50:53], v[114:129]
	v_cvt_pk_bf16_f32 v2, v2, v3
	v_cvt_pk_bf16_f32 v3, v4, v5
	v_cvt_pk_bf16_f32 v4, v6, v7
	v_cvt_pk_bf16_f32 v5, v8, v9
	v_cvt_pk_bf16_f32 v6, v42, v43
	v_cvt_pk_bf16_f32 v7, v44, v45
	v_cvt_pk_bf16_f32 v8, v46, v47
	v_mfma_f32_32x32x16_bf16 v[98:113], v[82:85], v[50:53], v[98:113]
	ds_read_b128 v[22:25], v250 offset:14336
	ds_read_b128 v[50:53], v250 offset:11264
	ds_read_b128 v[10:13], v250
	v_cvt_pk_bf16_f32 v9, v48, v49
	v_cvt_pk_bf16_f32 v54, v90, v91
	v_cvt_pk_bf16_f32 v55, v92, v93
	v_cvt_pk_bf16_f32 v56, v94, v95
	v_cvt_pk_bf16_f32 v57, v96, v97
	s_waitcnt lgkmcnt(3)
	v_mfma_f32_32x32x16_bf16 v[114:129], v[58:61], v[18:21], v[114:129]
	v_cvt_pk_bf16_f32 v58, v34, v35
	v_cvt_pk_bf16_f32 v59, v36, v37
	ds_read_b128 v[34:37], v250 offset:15360
	v_cvt_pk_bf16_f32 v60, v38, v39
	v_cvt_pk_bf16_f32 v61, v40, v41
	v_cvt_pk_bf16_f32 v202, v66, v67
	v_cvt_pk_bf16_f32 v203, v68, v69
	s_waitcnt lgkmcnt(3)
	v_mfma_f32_32x32x16_bf16 v[98:113], v[22:25], v[18:21], v[98:113]
	v_cvt_pk_bf16_f32 v18, v26, v27
	v_cvt_pk_bf16_f32 v19, v28, v29
	v_cvt_pk_bf16_f32 v20, v30, v31
	v_cvt_pk_bf16_f32 v21, v32, v33
	v_cvt_pk_bf16_f32 v204, v70, v71
	v_cvt_pk_bf16_f32 v205, v72, v73
	v_cvt_pk_bf16_f32 v82, v74, v75
	s_waitcnt lgkmcnt(2)
	v_mfma_f32_32x32x16_bf16 v[114:129], v[50:53], v[18:21], v[114:129]
	v_cvt_pk_bf16_f32 v83, v76, v77
	v_cvt_pk_bf16_f32 v84, v78, v79
	v_cvt_pk_bf16_f32 v85, v80, v81
	s_lshl_b32 s2, s20, 6
	s_mov_b32 s41, 1
	s_mov_b64 s[20:21], 0
	s_nop 5
	v_max3_f32 v14, v114, s38, v115
	s_waitcnt lgkmcnt(0)
	v_mfma_f32_32x32x16_bf16 v[98:113], v[34:37], v[18:21], v[98:113]
	ds_read_b128 v[50:53], v250 offset:1024
	ds_read_b128 v[18:21], v250 offset:4096
	ds_read_b128 v[62:65], v250 offset:5120
	v_max3_f32 v14, v14, v116, v117
	v_max3_f32 v14, v14, v118, v119
	v_max3_f32 v14, v14, v120, v121
	v_max3_f32 v14, v14, v122, v123
	v_max3_f32 v14, v14, v124, v125
	v_max3_f32 v14, v14, v126, v127
	v_mfma_f32_32x32x16_bf16 v[34:49], v[214:217], v[10:13], 0
	v_max3_f32 v14, v14, v128, v129
	s_nop 0
	v_max3_f32 v14, v14, v98, v99
	v_max3_f32 v14, v14, v100, v101
	v_max3_f32 v14, v14, v102, v103
	v_max3_f32 v14, v14, v104, v105
	v_max3_f32 v14, v14, v106, v107
	v_max3_f32 v14, v14, v108, v109
	s_waitcnt lgkmcnt(1)
	v_mfma_f32_32x32x16_bf16 v[18:33], v[214:217], v[18:21], 0
	v_max3_f32 v14, v14, v110, v111
	v_max3_f32 v14, v14, v112, v113
	v_mov_b32_e32 v15, v14
	ds_read_b128 v[10:13], v250 offset:2048
	ds_read_b128 v[66:69], v250 offset:3072
	ds_read_b128 v[70:73], v250 offset:6144
	ds_read_b128 v[74:77], v250 offset:7168
	v_permlane32_swap_b32_e32 v14, v15
	v_max_f32_e32 v15, v15, v15
	v_mfma_f32_32x32x16_bf16 v[34:49], v[54:57], v[50:53], v[34:49]
	v_max_f32_e32 v14, v14, v14
	v_max_f32_e32 v14, v14, v15
	v_mul_f32_e32 v14, 0xbe38aa3b, v14
	v_fmamk_f32 v15, v114, 0x3e38aa3b, v14
	v_fmamk_f32 v50, v118, 0x3e38aa3b, v14
	v_exp_f32_e32 v50, v50
	v_fmamk_f32 v51, v119, 0x3e38aa3b, v14
	s_waitcnt lgkmcnt(4)
	v_mfma_f32_32x32x16_bf16 v[18:33], v[54:57], v[62:65], v[18:33]
	v_exp_f32_e32 v51, v51
	v_fmamk_f32 v52, v120, 0x3e38aa3b, v14
	v_exp_f32_e32 v52, v52
	v_fmamk_f32 v53, v121, 0x3e38aa3b, v14
	v_exp_f32_e32 v53, v53
	v_fmamk_f32 v109, v109, 0x3e38aa3b, v14
	s_waitcnt lgkmcnt(3)
	v_mfma_f32_32x32x16_bf16 v[34:49], v[58:61], v[10:13], v[34:49]
	v_exp_f32_e32 v10, v15
	v_fmamk_f32 v11, v115, 0x3e38aa3b, v14
	v_exp_f32_e32 v11, v11
	v_fmamk_f32 v12, v116, 0x3e38aa3b, v14
	v_exp_f32_e32 v12, v12
	v_fmamk_f32 v15, v117, 0x3e38aa3b, v14
	v_exp_f32_e32 v15, v15
	s_waitcnt lgkmcnt(1)
	v_mfma_f32_32x32x16_bf16 v[18:33], v[58:61], v[70:73], v[18:33]
	v_add_f32_e32 v13, 0, v10
	v_add_f32_e32 v13, v13, v11
	v_add_f32_e32 v13, v13, v12
	v_add_f32_e32 v13, v13, v15
	v_add_f32_e32 v13, v13, v50
	v_add_f32_e32 v13, v13, v51
	v_cvt_pk_bf16_f32 v10, v10, v11
	v_mfma_f32_32x32x16_bf16 v[34:49], v[6:9], v[66:69], v[34:49]
	v_cvt_pk_bf16_f32 v11, v12, v15
	v_cvt_pk_bf16_f32 v12, v50, v51
	s_waitcnt lgkmcnt(0)
	v_mfma_f32_32x32x16_bf16 v[18:33], v[6:9], v[74:77], v[18:33]
	v_fmamk_f32 v6, v122, 0x3e38aa3b, v14
	v_exp_f32_e32 v89, v6
	v_fmamk_f32 v6, v123, 0x3e38aa3b, v14
	v_exp_f32_e32 v94, v6
	v_fmamk_f32 v7, v124, 0x3e38aa3b, v14
	v_add_f32_e32 v6, v13, v52
	v_exp_f32_e32 v95, v7
	v_fmamk_f32 v7, v125, 0x3e38aa3b, v14
	v_add_f32_e32 v6, v6, v53
	v_exp_f32_e32 v96, v7
	v_fmamk_f32 v7, v126, 0x3e38aa3b, v14
	v_add_f32_e32 v6, v6, v89
	v_exp_f32_e32 v97, v7
	v_fmamk_f32 v7, v127, 0x3e38aa3b, v14
	v_add_f32_e32 v6, v6, v94
	v_exp_f32_e32 v114, v7
	v_fmamk_f32 v7, v128, 0x3e38aa3b, v14
	v_add_f32_e32 v6, v6, v95
	v_exp_f32_e32 v115, v7
	v_fmamk_f32 v7, v129, 0x3e38aa3b, v14
	v_add_f32_e32 v6, v6, v96
	v_exp_f32_e32 v116, v7
	v_fmamk_f32 v7, v98, 0x3e38aa3b, v14
	v_add_f32_e32 v6, v6, v97
	v_exp_f32_e32 v98, v7
	v_fmamk_f32 v7, v99, 0x3e38aa3b, v14
	v_add_f32_e32 v6, v6, v114
	v_exp_f32_e32 v99, v7
	v_fmamk_f32 v7, v100, 0x3e38aa3b, v14
	v_add_f32_e32 v6, v6, v115
	v_exp_f32_e32 v100, v7
	v_fmamk_f32 v7, v101, 0x3e38aa3b, v14
	v_add_f32_e32 v6, v6, v116
	v_exp_f32_e32 v101, v7
	v_fmamk_f32 v7, v102, 0x3e38aa3b, v14
	v_add_f32_e32 v6, v6, v98
	v_exp_f32_e32 v102, v7
	v_fmamk_f32 v7, v103, 0x3e38aa3b, v14
	v_add_f32_e32 v6, v6, v99
	v_exp_f32_e32 v103, v7
	v_add_f32_e32 v6, v6, v100
	v_add_f32_e32 v6, v6, v101
	v_add_f32_e32 v6, v6, v102
	v_add_f32_e32 v54, v6, v103
	v_fmamk_f32 v6, v104, 0x3e38aa3b, v14
	v_exp_f32_e32 v104, v6
	ds_read_b128 v[6:9], v250 offset:16384
	v_fmamk_f32 v13, v105, 0x3e38aa3b, v14
	v_exp_f32_e32 v105, v13
	v_cvt_pk_bf16_f32 v13, v52, v53
	ds_read_b128 v[50:53], v250 offset:18432
	ds_read_b128 v[90:93], v250 offset:17408
	s_waitcnt lgkmcnt(2)
	v_mfma_f32_32x32x16_bf16 v[66:81], v[6:9], v[10:13], 0
	v_add_f32_e32 v6, v54, v104
	v_add_f32_e32 v15, v6, v105
	v_fmamk_f32 v6, v106, 0x3e38aa3b, v14
	v_exp_f32_e32 v106, v6
	v_fmamk_f32 v6, v107, 0x3e38aa3b, v14
	v_exp_f32_e32 v107, v6
	ds_read_b128 v[6:9], v250 offset:19456
	s_waitcnt lgkmcnt(2)
	v_mfma_f32_32x32x16_bf16 v[50:65], v[50:53], v[10:13], 0
	v_fmamk_f32 v10, v108, 0x3e38aa3b, v14
	v_exp_f32_e32 v108, v10
	v_cvt_pk_bf16_f32 v10, v89, v94
	v_cvt_pk_bf16_f32 v11, v95, v96
	v_cvt_pk_bf16_f32 v12, v97, v114
	v_cvt_pk_bf16_f32 v13, v115, v116
	v_fmamk_f32 v94, v110, 0x3e38aa3b, v14
	v_exp_f32_e32 v89, v109
	s_waitcnt lgkmcnt(1)
	v_mfma_f32_32x32x16_bf16 v[66:81], v[90:93], v[10:13], v[66:81]
	ds_read_b128 v[90:93], v250 offset:20480
	v_exp_f32_e32 v109, v94
	v_add_f32_e32 v15, v15, v106
	v_add_f32_e32 v15, v15, v107
	v_add_f32_e32 v15, v15, v108
	v_add_f32_e32 v15, v15, v89
	v_add_f32_e32 v15, v15, v109
	s_waitcnt lgkmcnt(1)
	v_mfma_f32_32x32x16_bf16 v[50:65], v[6:9], v[10:13], v[50:65]
	v_cvt_pk_bf16_f32 v6, v98, v99
	v_cvt_pk_bf16_f32 v7, v100, v101
	v_cvt_pk_bf16_f32 v8, v102, v103
	v_cvt_pk_bf16_f32 v9, v104, v105
	ds_read_b128 v[10:13], v250 offset:22528
	ds_read_b128 v[94:97], v250 offset:21504
	s_waitcnt lgkmcnt(2)
	v_mfma_f32_32x32x16_bf16 v[66:81], v[90:93], v[6:9], v[66:81]
	v_fmamk_f32 v90, v111, 0x3e38aa3b, v14
	v_exp_f32_e32 v98, v90
	v_fmamk_f32 v90, v112, 0x3e38aa3b, v14
	v_fmac_f32_e32 v14, 0x3e38aa3b, v113
	v_exp_f32_e32 v99, v90
	ds_read_b128 v[90:93], v250 offset:23552
	v_add_f32_e32 v15, v15, v98
	s_waitcnt lgkmcnt(2)
	v_mfma_f32_32x32x16_bf16 v[50:65], v[10:13], v[6:9], v[50:65]
	v_exp_f32_e32 v11, v14
	v_add_f32_e32 v10, v15, v99
	v_cvt_pk_bf16_f32 v6, v106, v107
	v_cvt_pk_bf16_f32 v7, v108, v89
	v_cvt_pk_bf16_f32 v8, v109, v98
	v_cvt_pk_bf16_f32 v9, v99, v11
	v_add_f32_e32 v10, v10, v11
	v_mov_b32_e32 v11, v10
	s_waitcnt lgkmcnt(1)
	v_mfma_f32_32x32x16_bf16 v[66:81], v[94:97], v[6:9], v[66:81]
	v_permlane32_swap_b32_e32 v10, v11
	v_add_f32_e32 v10, v10, v11
	v_rcp_f32_e32 v10, v10
	v_cvt_pk_bf16_f32 v89, v16, v17
	v_ashrrev_i32_e32 v118, 3, v210
	v_and_b32_e32 v118, 0xffffffe0, v118
	v_ashrrev_i32_e32 v119, 31, v118
	v_bfe_u32 v120, v210, 6, 1
	v_lshl_add_u64 v[118:119], s[16:17], 0, v[118:119]
	v_lshl_or_b32 v118, v120, 4, v118
	v_or_b32_e32 v118, v118, v211
	v_ashrrev_i32_e32 v120, 7, v210
	v_lshlrev_b64 v[118:119], 10, v[118:119]
	v_and_b32_e32 v120, 1, v120
	v_lshl_add_u64 v[118:119], v[118:119], 0, s[2:3]
	v_lshl_or_b32 v118, v120, 5, v118
	v_or_b32_e32 v118, v118, v1
	v_lshlrev_b64 v[118:119], 2, v[118:119]
	v_lshl_add_u64 v[118:119], s[12:13], 0, v[118:119]
	global_load_dword v110, v[118:119], off
	v_add_co_u32_e32 v120, vcc, s26, v118
	s_nop 1
	v_addc_co_u32_e32 v121, vcc, 0, v119, vcc
	global_load_dword v111, v[120:121], off offset:-4096
	global_load_dword v112, v[120:121], off
	v_add_co_u32_e32 v120, vcc, s39, v118
	s_nop 1
	v_addc_co_u32_e32 v121, vcc, 0, v119, vcc
	global_load_dword v113, v[120:121], off offset:-4096
	global_load_dword v114, v[120:121], off
	v_add_co_u32_e32 v120, vcc, s40, v118
	s_nop 1
	v_addc_co_u32_e32 v121, vcc, 0, v119, vcc
	global_load_dword v115, v[120:121], off offset:-4096
	global_load_dword v116, v[120:121], off
	v_add_co_u32_e32 v120, vcc, s29, v118
	s_nop 1
	v_addc_co_u32_e32 v121, vcc, 0, v119, vcc
	global_load_dword v117, v[120:121], off
	s_nop 6
	s_waitcnt vmcnt(35)
	v_fmac_f32_e32 v245, v10, v70
	s_waitcnt lgkmcnt(0)
	v_mfma_f32_32x32x16_bf16 v[50:65], v[90:93], v[6:9], v[50:65]
	v_lshl_add_u64 v[6:7], v[208:209], 2, s[4:5]
	v_add_co_u32_e32 v8, vcc, s26, v6
	s_waitcnt vmcnt(34)
	v_fmac_f32_e32 v243, v10, v71
	v_addc_co_u32_e32 v9, vcc, 0, v7, vcc
	s_waitcnt vmcnt(33)
	v_fmac_f32_e32 v241, v10, v72
	s_waitcnt vmcnt(32)
	v_fmac_f32_e32 v239, v10, v73
	global_store_dword v[8:9], v245, off nt
	global_store_dword v[8:9], v243, off offset:1024 nt
	global_store_dword v[8:9], v241, off offset:2048 nt
	global_store_dword v[8:9], v239, off offset:3072 nt
	v_add_co_u32_e32 v8, vcc, s30, v6
	s_waitcnt vmcnt(35)
	v_fmac_f32_e32 v244, v10, v74
	v_addc_co_u32_e32 v9, vcc, 0, v7, vcc
	s_waitcnt vmcnt(34)
	v_fmac_f32_e32 v242, v10, v75
	s_waitcnt vmcnt(33)
	v_fmac_f32_e32 v240, v10, v76
	s_waitcnt vmcnt(32)
	v_fmac_f32_e32 v238, v10, v77
	global_store_dword v[8:9], v244, off nt
	global_store_dword v[8:9], v242, off offset:1024 nt
	global_store_dword v[8:9], v240, off offset:2048 nt
	global_store_dword v[8:9], v238, off offset:3072 nt
	v_add_co_u32_e32 v8, vcc, s27, v6
	s_waitcnt vmcnt(35)
	v_fmac_f32_e32 v236, v10, v78
	v_addc_co_u32_e32 v9, vcc, 0, v7, vcc
	s_waitcnt vmcnt(34)
	v_fmac_f32_e32 v234, v10, v79
	s_waitcnt vmcnt(31)
	v_fmac_f32_e32 v232, v10, v80
	s_waitcnt vmcnt(30)
	v_fmac_f32_e32 v230, v10, v81
	global_store_dword v[8:9], v236, off nt
	global_store_dword v[8:9], v234, off offset:1024 nt
	global_store_dword v[8:9], v232, off offset:2048 nt
	global_store_dword v[8:9], v230, off offset:3072 nt
	v_add_co_u32_e32 v8, vcc, s34, v6
	v_fmac_f32_e32 v237, v10, v50
	v_addc_co_u32_e32 v9, vcc, 0, v7, vcc
	v_fmac_f32_e32 v235, v10, v51
	s_waitcnt vmcnt(33)
	v_fmac_f32_e32 v233, v10, v52
	s_waitcnt vmcnt(32)
	v_fmac_f32_e32 v231, v10, v53
	global_store_dword v[8:9], v237, off nt
	global_store_dword v[8:9], v235, off offset:1024 nt
	global_store_dword v[8:9], v233, off offset:2048 nt
	global_store_dword v[8:9], v231, off offset:3072 nt
	v_add_co_u32_e32 v8, vcc, s35, v6
	s_waitcnt vmcnt(35)
	v_fmac_f32_e32 v228, v10, v54
	v_addc_co_u32_e32 v9, vcc, 0, v7, vcc
	s_waitcnt vmcnt(34)
	v_fmac_f32_e32 v226, v10, v55
	s_waitcnt vmcnt(33)
	v_fmac_f32_e32 v224, v10, v56
	s_waitcnt vmcnt(32)
	v_fmac_f32_e32 v222, v10, v57
	global_store_dword v[8:9], v228, off nt
	global_store_dword v[8:9], v226, off offset:1024 nt
	global_store_dword v[8:9], v224, off offset:2048 nt
	global_store_dword v[8:9], v222, off offset:3072 nt
	v_add_co_u32_e32 v8, vcc, s36, v6
	v_fmac_f32_e32 v249, v10, v66
	v_fmac_f32_e32 v248, v10, v67
	v_fmac_f32_e32 v247, v10, v68
	v_fmac_f32_e32 v246, v10, v69
	v_addc_co_u32_e32 v9, vcc, 0, v7, vcc
	global_store_dword v[6:7], v249, off nt
	global_store_dword v[6:7], v248, off offset:1024 nt
	global_store_dword v[6:7], v247, off offset:2048 nt
	global_store_dword v[6:7], v246, off offset:3072 nt
	v_add_co_u32_e32 v6, vcc, s37, v6
	s_waitcnt vmcnt(35)
	v_fmac_f32_e32 v221, v10, v62
	v_addc_co_u32_e32 v7, vcc, 0, v7, vcc
	s_waitcnt vmcnt(34)
	v_fmac_f32_e32 v220, v10, v63
	s_waitcnt vmcnt(33)
	v_fmac_f32_e32 v219, v10, v64
	s_waitcnt vmcnt(32)
	v_fmac_f32_e32 v218, v10, v65
	global_store_dword v[6:7], v221, off nt
	global_store_dword v[6:7], v220, off offset:1024 nt
	global_store_dword v[6:7], v219, off offset:2048 nt
	global_store_dword v[6:7], v218, off offset:3072 nt
	v_max3_f32 v6, v34, s38, v35
	v_max3_f32 v6, v6, v36, v37
	v_max3_f32 v6, v6, v38, v39
	v_max3_f32 v6, v6, v40, v41
	v_max3_f32 v7, v18, s38, v19
	v_max3_f32 v6, v6, v42, v43
	v_max3_f32 v7, v7, v20, v21
	v_max3_f32 v6, v6, v44, v45
	v_max3_f32 v7, v7, v22, v23
	v_max3_f32 v6, v6, v46, v47
	v_max3_f32 v7, v7, v24, v25
	v_fmac_f32_e32 v229, v10, v58
	v_fmac_f32_e32 v227, v10, v59
	v_fmac_f32_e32 v225, v10, v60
	v_fmac_f32_e32 v223, v10, v61
	v_max3_f32 v6, v6, v48, v49
	v_max3_f32 v7, v7, v26, v27
	global_store_dword v[8:9], v229, off nt
	global_store_dword v[8:9], v227, off offset:1024 nt
	global_store_dword v[8:9], v225, off offset:2048 nt
	global_store_dword v[8:9], v223, off offset:3072 nt
	v_max3_f32 v7, v7, v28, v29
	v_mov_b32_e32 v8, v6
	v_max3_f32 v7, v7, v30, v31
	s_nop 0
	v_permlane32_swap_b32_e32 v6, v8
	v_max3_f32 v7, v7, v32, v33
	v_max_f32_e32 v8, v8, v8
	v_max_f32_e32 v6, v6, v6
	v_max_f32_e32 v90, v6, v8
	v_mov_b32_e32 v6, v7
	s_nop 1
	v_permlane32_swap_b32_e32 v7, v6
	v_mul_f32_e32 v8, 0xbe38aa3b, v90
	v_fmamk_f32 v9, v34, 0x3e38aa3b, v8
	v_max_f32_e32 v6, v6, v6
	v_max_f32_e32 v7, v7, v7
	v_exp_f32_e32 v9, v9
	v_max_f32_e32 v91, v7, v6
	v_fmamk_f32 v7, v35, 0x3e38aa3b, v8
	v_exp_f32_e32 v7, v7
	v_fmamk_f32 v10, v36, 0x3e38aa3b, v8
	v_exp_f32_e32 v10, v10
	v_fmamk_f32 v11, v37, 0x3e38aa3b, v8
	v_exp_f32_e32 v11, v11
	v_fmamk_f32 v12, v38, 0x3e38aa3b, v8
	v_add_f32_e32 v6, 0, v9
	v_exp_f32_e32 v12, v12
	v_fmamk_f32 v13, v39, 0x3e38aa3b, v8
	v_add_f32_e32 v6, v6, v7
	v_exp_f32_e32 v13, v13
	v_fmamk_f32 v14, v40, 0x3e38aa3b, v8
	v_add_f32_e32 v6, v6, v10
	v_exp_f32_e32 v14, v14
	v_fmamk_f32 v15, v41, 0x3e38aa3b, v8
	v_fmamk_f32 v16, v42, 0x3e38aa3b, v8
	v_add_f32_e32 v6, v6, v11
	v_exp_f32_e32 v15, v15
	v_exp_f32_e32 v92, v16
	v_fmamk_f32 v16, v43, 0x3e38aa3b, v8
	v_add_f32_e32 v6, v6, v12
	v_exp_f32_e32 v93, v16
	v_fmamk_f32 v16, v44, 0x3e38aa3b, v8
	v_add_f32_e32 v6, v6, v13
	v_exp_f32_e32 v94, v16
	v_fmamk_f32 v16, v45, 0x3e38aa3b, v8
	v_add_f32_e32 v6, v6, v14
	v_exp_f32_e32 v95, v16
	v_fmamk_f32 v16, v46, 0x3e38aa3b, v8
	v_add_f32_e32 v6, v6, v15
	v_exp_f32_e32 v96, v16
	v_fmamk_f32 v16, v47, 0x3e38aa3b, v8
	v_add_f32_e32 v6, v6, v92
	v_exp_f32_e32 v97, v16
	v_fmamk_f32 v16, v48, 0x3e38aa3b, v8
	v_add_f32_e32 v6, v6, v93
	v_exp_f32_e32 v98, v16
	v_fmac_f32_e32 v8, 0x3e38aa3b, v49
	v_mul_f32_e32 v16, 0xbe38aa3b, v91
	v_add_f32_e32 v6, v6, v94
	v_exp_f32_e32 v99, v8
	v_fmamk_f32 v8, v18, 0x3e38aa3b, v16
	v_add_f32_e32 v6, v6, v95
	v_exp_f32_e32 v17, v8
	v_fmamk_f32 v8, v19, 0x3e38aa3b, v16
	v_add_f32_e32 v6, v6, v96
	v_exp_f32_e32 v18, v8
	v_fmamk_f32 v8, v20, 0x3e38aa3b, v16
	v_add_f32_e32 v6, v6, v97
	v_exp_f32_e32 v19, v8
	v_fmamk_f32 v8, v21, 0x3e38aa3b, v16
	v_add_f32_e32 v6, v6, v98
	v_exp_f32_e32 v20, v8
	v_fmamk_f32 v8, v22, 0x3e38aa3b, v16
	v_add_f32_e32 v100, v6, v99
	v_add_f32_e32 v6, 0, v17
	v_exp_f32_e32 v21, v8
	v_fmamk_f32 v8, v23, 0x3e38aa3b, v16
	v_add_f32_e32 v6, v6, v18
	v_exp_f32_e32 v22, v8
	v_fmamk_f32 v8, v24, 0x3e38aa3b, v16
	v_add_f32_e32 v6, v6, v19
	v_exp_f32_e32 v23, v8
	v_fmamk_f32 v8, v25, 0x3e38aa3b, v16
	v_add_f32_e32 v6, v6, v20
	v_exp_f32_e32 v24, v8
	v_fmamk_f32 v8, v26, 0x3e38aa3b, v16
	v_add_f32_e32 v6, v6, v21
	v_exp_f32_e32 v25, v8
	v_add_f32_e32 v6, v6, v22
	v_add_f32_e32 v6, v6, v23
	v_add_f32_e32 v6, v6, v24
	v_add_f32_e32 v26, v6, v25
	v_fmamk_f32 v6, v27, 0x3e38aa3b, v16
	v_exp_f32_e32 v27, v6
	v_cvt_pk_bf16_f32 v6, v9, v7
	v_cvt_pk_bf16_f32 v7, v10, v11
	v_fmamk_f32 v10, v28, 0x3e38aa3b, v16
	v_cvt_pk_bf16_f32 v9, v14, v15
	v_exp_f32_e32 v28, v10
	v_fmamk_f32 v14, v29, 0x3e38aa3b, v16
	v_cvt_pk_bf16_f32 v8, v12, v13
	v_cvt_pk_bf16_f32 v13, v23, v24
	v_exp_f32_e32 v23, v14
	v_fmamk_f32 v14, v30, 0x3e38aa3b, v16
	v_mfma_f32_32x32x16_bf16 v[66:81], v[202:205], v[6:9], 0
	v_exp_f32_e32 v24, v14
	v_add_f32_e32 v14, v26, v27
	v_add_f32_e32 v14, v14, v28
	v_add_f32_e32 v14, v14, v23
	v_cvt_pk_bf16_f32 v10, v17, v18
	v_cvt_pk_bf16_f32 v11, v19, v20
	v_cvt_pk_bf16_f32 v12, v21, v22
	v_mfma_f32_32x32x16_bf16 v[34:49], v[2:5], v[6:9], 0
	v_fmamk_f32 v6, v31, 0x3e38aa3b, v16
	v_exp_f32_e32 v26, v6
	v_add_f32_e32 v14, v14, v24
	v_fmamk_f32 v6, v32, 0x3e38aa3b, v16
	v_fmac_f32_e32 v16, 0x3e38aa3b, v33
	v_exp_f32_e32 v29, v6
	v_exp_f32_e32 v30, v16
	v_mfma_f32_32x32x16_bf16 v[50:65], v[202:205], v[10:13], 0
	v_add_f32_e32 v18, v14, v26
	v_mov_b32_e32 v22, v100
	s_nop 1
	v_permlane32_swap_b32_e32 v100, v22
	v_add_f32_e32 v32, v100, v22
	v_cvt_pk_bf16_f32 v22, v25, v27
	v_cvt_pk_bf16_f32 v23, v28, v23
	v_mfma_f32_32x32x16_bf16 v[2:17], v[2:5], v[10:13], 0
	v_cvt_pk_bf16_f32 v24, v24, v26
	v_cvt_pk_bf16_f32 v25, v29, v30
	v_lshlrev_b32_e32 v26, 2, v213
	v_lshl_or_b32 v27, v212, 10, v26
	v_add_f32_e32 v18, v18, v29
	v_add_u32_e32 v28, 0x10000, v27
	v_add_f32_e32 v31, v18, v30
	v_mfma_f32_32x32x16_bf16 v[2:17], v[86:89], v[22:25], v[2:17]
	ds_write_b32 v28, v90
	v_add_u32_e32 v28, 0x10100, v27
	v_cvt_pk_bf16_f32 v18, v92, v93
	v_cvt_pk_bf16_f32 v19, v94, v95
	v_cvt_pk_bf16_f32 v20, v96, v97
	v_cvt_pk_bf16_f32 v21, v98, v99
	ds_write_b32 v28, v32
	v_mov_b32_e32 v28, v31
	v_mfma_f32_32x32x16_bf16 v[66:81], v[82:85], v[18:21], v[66:81]
	s_nop 0
	v_permlane32_swap_b32_e32 v31, v28
	s_nop 0
	v_cvt_pk_bf16_f32 v2, v2, v3
	v_cvt_pk_bf16_f32 v3, v4, v5
	v_cvt_pk_bf16_f32 v4, v6, v7
	v_cvt_pk_bf16_f32 v5, v8, v9
	v_mfma_f32_32x32x16_bf16 v[34:49], v[86:89], v[18:21], v[34:49]
	v_add_u32_e32 v19, 0x10200, v27
	v_add_f32_e32 v18, v31, v28
	ds_write_b32 v19, v91
	v_add_u32_e32 v19, 0x10300, v27
	ds_write_b32 v19, v18
	v_cvt_pk_bf16_f32 v18, v66, v67
	v_cvt_pk_bf16_f32 v19, v68, v69
	v_mfma_f32_32x32x16_bf16 v[50:65], v[82:85], v[22:25], v[50:65]
	v_lshl_or_b32 v22, v212, 13, v206
	ds_write_b128 v22, v[2:5] offset:6144
	v_cvt_pk_bf16_f32 v2, v10, v11
	v_cvt_pk_bf16_f32 v3, v12, v13
	v_cvt_pk_bf16_f32 v4, v14, v15
	v_cvt_pk_bf16_f32 v5, v16, v17
	ds_write_b128 v22, v[2:5] offset:7168
	v_ashrrev_i32_e32 v2, 3, v210
	v_and_b32_e32 v2, 0xffffffe0, v2
	v_ashrrev_i32_e32 v3, 31, v2
	v_bfe_u32 v16, v210, 6, 1
	v_lshl_add_u64 v[2:3], s[16:17], 0, v[2:3]
	v_lshl_or_b32 v2, v16, 4, v2
	v_or_b32_e32 v2, v2, v211
	v_ashrrev_i32_e32 v14, 7, v210
	v_lshlrev_b64 v[2:3], 10, v[2:3]
	v_and_b32_e32 v15, 1, v14
	v_lshl_add_u64 v[2:3], v[2:3], 0, s[2:3]
	v_lshl_or_b32 v2, v15, 5, v2
	v_or_b32_e32 v2, v2, v1
	v_lshlrev_b64 v[2:3], 2, v[2:3]
	v_cvt_pk_bf16_f32 v20, v70, v71
	v_cvt_pk_bf16_f32 v21, v72, v73
	ds_write_b128 v22, v[18:21]
	v_cvt_pk_bf16_f32 v18, v74, v75
	v_cvt_pk_bf16_f32 v19, v76, v77
	v_cvt_pk_bf16_f32 v20, v78, v79
	v_cvt_pk_bf16_f32 v21, v80, v81
	ds_write_b128 v22, v[18:21] offset:1024
	v_cvt_pk_bf16_f32 v18, v50, v51
	v_cvt_pk_bf16_f32 v19, v52, v53
	v_cvt_pk_bf16_f32 v20, v54, v55
	v_cvt_pk_bf16_f32 v21, v56, v57
	ds_write_b128 v22, v[18:21] offset:2048
	v_cvt_pk_bf16_f32 v18, v58, v59
	v_cvt_pk_bf16_f32 v19, v60, v61
	v_cvt_pk_bf16_f32 v20, v62, v63
	v_cvt_pk_bf16_f32 v21, v64, v65
	ds_write_b128 v22, v[18:21] offset:3072
	v_cvt_pk_bf16_f32 v18, v34, v35
	v_cvt_pk_bf16_f32 v19, v36, v37
	v_cvt_pk_bf16_f32 v20, v38, v39
	v_cvt_pk_bf16_f32 v21, v40, v41
	ds_write_b128 v22, v[18:21] offset:4096
	v_cvt_pk_bf16_f32 v18, v42, v43
	v_cvt_pk_bf16_f32 v19, v44, v45
	v_cvt_pk_bf16_f32 v20, v46, v47
	v_cvt_pk_bf16_f32 v21, v48, v49
	ds_write_b128 v22, v[18:21] offset:5120
	v_lshl_add_u64 v[2:3], s[14:15], 0, v[2:3]
	v_lshl_or_b32 v4, v15, 9, v26
	v_or_b32_e32 v5, 0x10000, v4
	v_or_b32_e32 v12, 0x10d00, v4
	s_waitcnt lgkmcnt(0)
	s_barrier
	v_or_b32_e32 v6, 0x10100, v4
	v_or_b32_e32 v7, 0x10400, v4
	v_or_b32_e32 v8, 0x10500, v4
	v_or_b32_e32 v9, 0x10800, v4
	v_or_b32_e32 v10, 0x10900, v4
	v_or_b32_e32 v11, 0x10c00, v4
	ds_read_b32 v5, v5
	ds_read_b32 v13, v6
	ds_read_b32 v15, v7
	ds_read_b32 v24, v8
	ds_read_b32 v25, v9
	ds_read_b32 v26, v10
	ds_read_b32 v27, v11
	ds_read_b32 v12, v12
	v_or_b32_e32 v6, 0x11000, v4
	v_or_b32_e32 v7, 0x11100, v4
	v_or_b32_e32 v8, 0x11400, v4
	v_or_b32_e32 v9, 0x11500, v4
	v_or_b32_e32 v10, 0x11800, v4
	v_or_b32_e32 v11, 0x11900, v4
	v_or_b32_e32 v28, 0x11c00, v4
	v_or_b32_e32 v4, 0x11d00, v4
	ds_read_b32 v29, v6
	ds_read_b32 v30, v7
	ds_read_b32 v31, v8
	ds_read_b32 v32, v9
	ds_read_b32 v33, v10
	ds_read_b32 v34, v11
	ds_read_b32 v28, v28
	ds_read_b32 v35, v4
	s_waitcnt lgkmcnt(13)
	v_max_f32_e32 v4, v15, v15
	v_max_f32_e32 v6, v5, v5
	v_max_f32_e32 v4, v6, v4
	s_waitcnt lgkmcnt(9)
	v_max3_f32 v4, v4, v25, v27
	s_waitcnt lgkmcnt(5)
	v_max3_f32 v4, v4, v29, v31
	s_waitcnt lgkmcnt(1)
	v_max3_f32 v36, v4, v33, v28
	v_sub_f32_e32 v4, v5, v36
	v_mul_f32_e32 v4, 0x3e38aa3b, v4
	v_exp_f32_e32 v37, v4
	v_lshlrev_b32_e32 v4, 11, v14
	v_lshlrev_b32_e32 v5, 10, v16
	v_or3_b32 v14, v206, v4, v5
	ds_read_b128 v[4:7], v14
	ds_read_b128 v[8:11], v14 offset:8192
	v_fma_f32 v13, v13, v37, 0
	s_waitcnt lgkmcnt(1)
	v_lshlrev_b32_e32 v16, 16, v4
	v_and_b32_e32 v4, 0xffff0000, v4
	v_fma_f32 v38, v37, v4, 0
	v_lshlrev_b32_e32 v4, 16, v5
	v_fma_f32 v39, v37, v4, 0
	v_and_b32_e32 v4, 0xffff0000, v5
	v_sub_f32_e32 v5, v15, v36
	v_fma_f32 v40, v37, v4, 0
	v_lshlrev_b32_e32 v4, 16, v6
	v_mul_f32_e32 v5, 0x3e38aa3b, v5
	v_fma_f32 v41, v37, v4, 0
	v_and_b32_e32 v4, 0xffff0000, v6
	v_exp_f32_e32 v15, v5
	v_fma_f32 v42, v37, v4, 0
	v_lshlrev_b32_e32 v4, 16, v7
	v_fma_f32 v43, v37, v4, 0
	v_and_b32_e32 v4, 0xffff0000, v7
	v_fma_f32 v16, v37, v16, 0
	v_fma_f32 v37, v37, v4, 0
	s_waitcnt lgkmcnt(0)
	v_lshlrev_b32_e32 v4, 16, v8
	v_fmac_f32_e32 v16, v15, v4
	v_and_b32_e32 v4, 0xffff0000, v8
	v_fmac_f32_e32 v38, v15, v4
	v_lshlrev_b32_e32 v4, 16, v9
	v_fmac_f32_e32 v39, v15, v4
	v_and_b32_e32 v4, 0xffff0000, v9
	v_fmac_f32_e32 v40, v15, v4
	v_lshlrev_b32_e32 v4, 16, v10
	v_fmac_f32_e32 v41, v15, v4
	v_and_b32_e32 v4, 0xffff0000, v10
	v_fmac_f32_e32 v42, v15, v4
	v_lshlrev_b32_e32 v4, 16, v11
	v_fmac_f32_e32 v43, v15, v4
	v_sub_f32_e32 v4, v25, v36
	v_mul_f32_e32 v4, 0x3e38aa3b, v4
	v_fmac_f32_e32 v13, v24, v15
	v_exp_f32_e32 v24, v4
	ds_read_b128 v[4:7], v14 offset:16384
	v_and_b32_e32 v8, 0xffff0000, v11
	v_fmac_f32_e32 v37, v15, v8
	ds_read_b128 v[8:11], v14 offset:24576
	v_fmac_f32_e32 v13, v26, v24
	s_waitcnt lgkmcnt(1)
	v_lshlrev_b32_e32 v15, 16, v4
	v_and_b32_e32 v4, 0xffff0000, v4
	v_fmac_f32_e32 v38, v24, v4
	v_lshlrev_b32_e32 v4, 16, v5
	v_fmac_f32_e32 v39, v24, v4
	v_and_b32_e32 v4, 0xffff0000, v5
	v_sub_f32_e32 v5, v27, v36
	v_fmac_f32_e32 v40, v24, v4
	v_lshlrev_b32_e32 v4, 16, v6
	v_mul_f32_e32 v5, 0x3e38aa3b, v5
	v_fmac_f32_e32 v16, v24, v15
	v_fmac_f32_e32 v41, v24, v4
	v_and_b32_e32 v4, 0xffff0000, v6
	v_exp_f32_e32 v15, v5
	v_fmac_f32_e32 v42, v24, v4
	v_lshlrev_b32_e32 v4, 16, v7
	v_fmac_f32_e32 v43, v24, v4
	v_and_b32_e32 v4, 0xffff0000, v7
	v_fmac_f32_e32 v37, v24, v4
	s_waitcnt lgkmcnt(0)
	v_lshlrev_b32_e32 v4, 16, v8
	v_fmac_f32_e32 v16, v15, v4
	v_and_b32_e32 v4, 0xffff0000, v8
	v_fmac_f32_e32 v38, v15, v4
	v_lshlrev_b32_e32 v4, 16, v9
	v_fmac_f32_e32 v39, v15, v4
	v_and_b32_e32 v4, 0xffff0000, v9
	v_fmac_f32_e32 v40, v15, v4
	v_lshlrev_b32_e32 v4, 16, v10
	v_fmac_f32_e32 v41, v15, v4
	v_and_b32_e32 v4, 0xffff0000, v10
	v_fmac_f32_e32 v42, v15, v4
	v_lshlrev_b32_e32 v4, 16, v11
	v_fmac_f32_e32 v43, v15, v4
	v_sub_f32_e32 v4, v29, v36
	v_mul_f32_e32 v4, 0x3e38aa3b, v4
	v_fmac_f32_e32 v13, v12, v15
	v_exp_f32_e32 v12, v4
	ds_read_b128 v[4:7], v14 offset:32768
	v_and_b32_e32 v8, 0xffff0000, v11
	v_fmac_f32_e32 v37, v15, v8
	ds_read_b128 v[8:11], v14 offset:40960
	v_fmac_f32_e32 v13, v30, v12
	s_waitcnt lgkmcnt(1)
	v_lshlrev_b32_e32 v15, 16, v4
	v_and_b32_e32 v4, 0xffff0000, v4
	v_fmac_f32_e32 v38, v12, v4
	v_lshlrev_b32_e32 v4, 16, v5
	v_fmac_f32_e32 v39, v12, v4
	v_and_b32_e32 v4, 0xffff0000, v5
	v_sub_f32_e32 v5, v31, v36
	v_fmac_f32_e32 v40, v12, v4
	v_lshlrev_b32_e32 v4, 16, v6
	v_mul_f32_e32 v5, 0x3e38aa3b, v5
	v_fmac_f32_e32 v16, v12, v15
	v_fmac_f32_e32 v41, v12, v4
	v_and_b32_e32 v4, 0xffff0000, v6
	v_exp_f32_e32 v15, v5
	v_fmac_f32_e32 v42, v12, v4
	v_lshlrev_b32_e32 v4, 16, v7
	v_fmac_f32_e32 v43, v12, v4
	v_and_b32_e32 v4, 0xffff0000, v7
	v_fmac_f32_e32 v37, v12, v4
	s_waitcnt lgkmcnt(0)
	v_lshlrev_b32_e32 v4, 16, v8
	v_fmac_f32_e32 v16, v15, v4
	v_and_b32_e32 v4, 0xffff0000, v8
	v_fmac_f32_e32 v38, v15, v4
	v_lshlrev_b32_e32 v4, 16, v9
	v_fmac_f32_e32 v39, v15, v4
	v_and_b32_e32 v4, 0xffff0000, v9
	v_fmac_f32_e32 v40, v15, v4
	v_lshlrev_b32_e32 v4, 16, v10
	v_fmac_f32_e32 v41, v15, v4
	v_and_b32_e32 v4, 0xffff0000, v10
	v_fmac_f32_e32 v42, v15, v4
	v_lshlrev_b32_e32 v4, 16, v11
	v_fmac_f32_e32 v43, v15, v4
	v_sub_f32_e32 v4, v33, v36
	v_mul_f32_e32 v4, 0x3e38aa3b, v4
	v_exp_f32_e32 v12, v4
	ds_read_b128 v[4:7], v14 offset:49152
	v_and_b32_e32 v8, 0xffff0000, v11
	v_fmac_f32_e32 v37, v15, v8
	ds_read_b128 v[8:11], v14 offset:57344
	v_fmac_f32_e32 v13, v32, v15
	s_waitcnt lgkmcnt(1)
	v_lshlrev_b32_e32 v14, 16, v4
	v_and_b32_e32 v4, 0xffff0000, v4
	v_fmac_f32_e32 v38, v12, v4
	v_lshlrev_b32_e32 v4, 16, v5
	v_fmac_f32_e32 v39, v12, v4
	v_and_b32_e32 v4, 0xffff0000, v5
	v_sub_f32_e32 v5, v28, v36
	v_fmac_f32_e32 v40, v12, v4
	v_lshlrev_b32_e32 v4, 16, v6
	v_mul_f32_e32 v5, 0x3e38aa3b, v5
	v_fmac_f32_e32 v41, v12, v4
	v_and_b32_e32 v4, 0xffff0000, v6
	v_exp_f32_e32 v5, v5
	v_fmac_f32_e32 v42, v12, v4
	v_lshlrev_b32_e32 v4, 16, v7
	v_fmac_f32_e32 v43, v12, v4
	v_and_b32_e32 v4, 0xffff0000, v7
	v_fmac_f32_e32 v16, v12, v14
	v_fmac_f32_e32 v37, v12, v4
	s_waitcnt lgkmcnt(0)
	v_lshlrev_b32_e32 v4, 16, v8
	v_fmac_f32_e32 v16, v5, v4
	v_and_b32_e32 v4, 0xffff0000, v8
	v_fmac_f32_e32 v38, v5, v4
	v_lshlrev_b32_e32 v4, 16, v9
	v_fmac_f32_e32 v13, v34, v12
	v_fmac_f32_e32 v39, v5, v4
	v_and_b32_e32 v4, 0xffff0000, v9
	v_fmac_f32_e32 v13, v35, v5
	v_fmac_f32_e32 v40, v5, v4
	v_lshlrev_b32_e32 v4, 16, v10
	v_fmac_f32_e32 v41, v5, v4
	v_and_b32_e32 v4, 0xffff0000, v10
	v_rcp_f32_e32 v6, v13
	v_fmac_f32_e32 v42, v5, v4
	v_lshlrev_b32_e32 v4, 16, v11
	v_fmac_f32_e32 v43, v5, v4
	v_and_b32_e32 v4, 0xffff0000, v11
	v_fmac_f32_e32 v37, v5, v4
	v_add_co_u32_e32 v4, vcc, s26, v2
	s_waitcnt vmcnt(38)
	v_fmac_f32_e32 v111, v6, v38
	v_addc_co_u32_e32 v5, vcc, 0, v3, vcc
	s_waitcnt vmcnt(37)
	v_fmac_f32_e32 v112, v6, v39
	global_store_dword v[4:5], v111, off offset:-4096 nt
	global_store_dword v[4:5], v112, off nt
	v_add_co_u32_e32 v4, vcc, s29, v2
	s_waitcnt vmcnt(34)
	v_fmac_f32_e32 v117, v6, v40
	v_addc_co_u32_e32 v5, vcc, 0, v3, vcc
	global_store_dword v[4:5], v117, off nt
	v_add_co_u32_e32 v4, vcc, s34, v2
	v_fmac_f32_e32 v113, v6, v41
	s_nop 0
	v_addc_co_u32_e32 v5, vcc, 0, v3, vcc
	global_store_dword v[4:5], v113, off nt
	v_add_co_u32_e32 v4, vcc, 0x9000, v2
	v_fmac_f32_e32 v114, v6, v42
	s_nop 0
	v_addc_co_u32_e32 v5, vcc, 0, v3, vcc
	global_store_dword v[4:5], v114, off nt
	v_add_co_u32_e32 v4, vcc, 0xa000, v2
	v_fmac_f32_e32 v110, v6, v16
	s_nop 0
	v_addc_co_u32_e32 v5, vcc, 0, v3, vcc
	global_store_dword v[2:3], v110, off nt
	v_add_co_u32_e32 v2, vcc, 0xb000, v2
	v_fmac_f32_e32 v115, v6, v43
	s_nop 0
	v_addc_co_u32_e32 v3, vcc, 0, v3, vcc
	v_fmac_f32_e32 v116, v6, v37
	s_and_b64 vcc, exec, s[18:19]
	global_store_dword v[4:5], v115, off nt
	global_store_dword v[2:3], v116, off nt
	s_barrier
	s_cbranch_vccnz .LBB3_144
.LBB3_142:
	s_lshl_b32 s2, s41, 5
	s_add_i32 s2, s2, s22
	s_xor_b64 s[18:19], s[20:21], -1
	s_lshr_b32 s20, s2, 3
	v_mov_b32_e32 v210, v0
	s_add_i32 s20, s20, s24
	s_add_i32 s2, s20, s25
	v_ashrrev_i32_e32 v212, 6, v210
	v_lshl_add_u32 v2, s2, 3, v212
	v_ashrrev_i32_e32 v3, 31, v2
	v_and_b32_e32 v213, 63, v210
	v_lshlrev_b64 v[2:3], 15, v[2:3]
	v_lshl_add_u64 v[2:3], s[10:11], 0, v[2:3]
	v_lshlrev_b32_e32 v206, 4, v213
	v_lshl_add_u64 v[204:205], v[2:3], 0, v[206:207]
	v_and_b32_e32 v2, 3, v212
	v_lshlrev_b32_e32 v3, 3, v212
	v_and_or_b32 v214, v3, 32, v2
	v_and_b32_e32 v2, 0x3fffff8, v212
	v_add_u32_e32 v4, 8, v212
	v_or_b32_e32 v2, s23, v2
	v_and_b32_e32 v4, 0x3fffff8, v4
	v_or_b32_e32 v6, 8, v214
	v_lshlrev_b32_e32 v215, 6, v2
	v_or_b32_e32 v4, s23, v4
	v_or_b32_e32 v2, v6, v215
	v_lshlrev_b32_e32 v216, 6, v4
	v_lshlrev_b32_e32 v209, 10, v212
	v_ashrrev_i32_e32 v3, 31, v2
	v_or_b32_e32 v4, v216, v6
	v_or_b32_e32 v208, v206, v209
	v_lshl_add_u64 v[202:203], s[0:1], 0, v[206:207]
	v_lshlrev_b64 v[2:3], 10, v[2:3]
	v_ashrrev_i32_e32 v5, 31, v4
	s_waitcnt vmcnt(17)
	ds_write_b128 v208, v[190:193]
	s_waitcnt vmcnt(16)
	ds_write_b128 v208, v[194:197] offset:8192
	s_waitcnt vmcnt(15)
	ds_write_b128 v208, v[198:201] offset:16384
	v_lshl_add_u64 v[2:3], v[202:203], 0, v[2:3]
	v_lshlrev_b64 v[4:5], 10, v[4:5]
	v_lshl_add_u64 v[4:5], v[202:203], 0, v[4:5]
	global_load_dwordx4 v[98:101], v[2:3], off
	global_load_dwordx4 v[102:105], v[4:5], off
	v_add_u32_e32 v2, 16, v212
	v_and_b32_e32 v2, 0x3fffff8, v2
	v_or_b32_e32 v2, s23, v2
	v_lshlrev_b32_e32 v217, 6, v2
	v_or_b32_e32 v2, v217, v6
	v_ashrrev_i32_e32 v3, 31, v2
	v_lshlrev_b64 v[2:3], 10, v[2:3]
	v_lshl_add_u64 v[2:3], v[202:203], 0, v[2:3]
	global_load_dwordx4 v[106:109], v[2:3], off
	v_lshrrev_b32_e32 v2, 3, v210
	v_or_b32_e32 v10, 12, v214
	v_and_b32_e32 v211, 4, v2
	v_or_b32_e32 v2, v10, v215
	v_ashrrev_i32_e32 v3, 31, v2
	v_or_b32_e32 v4, v10, v216
	v_lshlrev_b64 v[2:3], 10, v[2:3]
	v_ashrrev_i32_e32 v5, 31, v4
	v_lshl_add_u64 v[2:3], v[202:203], 0, v[2:3]
	v_lshlrev_b64 v[4:5], 10, v[4:5]
	s_waitcnt lgkmcnt(0)
	s_barrier
	v_lshl_add_u64 v[4:5], v[202:203], 0, v[4:5]
	global_load_dwordx4 v[118:121], v[2:3], off
	global_load_dwordx4 v[122:125], v[4:5], off
	v_or_b32_e32 v2, v10, v217
	v_ashrrev_i32_e32 v3, 31, v2
	v_lshlrev_b64 v[2:3], 10, v[2:3]
	v_lshl_add_u64 v[2:3], v[202:203], 0, v[2:3]
	global_load_dwordx4 v[190:193], v[2:3], off
	v_lshlrev_b32_e32 v7, 2, v211
	v_or_b32_e32 v8, 0x1e000, v7
	v_or_b32_e32 v2, 0x1e040, v7
	v_or_b32_e32 v9, 0x1e020, v7
	ds_read_b128 v[50:53], v8
	ds_read_b128 v[54:57], v9
	v_or_b32_e32 v3, 0x1e060, v7
	ds_read_b128 v[58:61], v2
	ds_read_b128 v[62:65], v3
	v_or_b32_e32 v2, 0x1e080, v7
	v_or_b32_e32 v3, 0x1e0a0, v7
	ds_read_b128 v[18:21], v2
	ds_read_b128 v[22:25], v3
	v_or_b32_e32 v2, 0x1e0c0, v7
	v_or_b32_e32 v3, 0x1e0e0, v7
	ds_read_b128 v[26:29], v2
	ds_read_b128 v[30:33], v3
	v_or_b32_e32 v2, 0x1e100, v7
	v_and_b32_e32 v1, 31, v210
	v_or_b32_e32 v3, 0x1e120, v7
	ds_read_b128 v[82:85], v2
	ds_read_b128 v[86:89], v3
	v_or_b32_e32 v2, 0x1e140, v7
	v_lshlrev_b32_e32 v6, 2, v1
	v_or_b32_e32 v3, 0x1e160, v7
	ds_read_b128 v[90:93], v2
	ds_read_b128 v[94:97], v3
	v_or_b32_e32 v2, 0x1e180, v7
	v_or_b32_e32 v3, 0x1e1a0, v7
	ds_read_b128 v[34:37], v2
	ds_read_b128 v[38:41], v3
	v_or_b32_e32 v2, 0x1e1c0, v7
	v_or_b32_e32 v4, 0x1e200, v6
	v_or_b32_e32 v3, 0x1e1e0, v7
	ds_read_b32 v66, v4
	ds_read_b128 v[42:45], v2
	ds_read_b128 v[46:49], v3
	v_or_b32_e32 v2, 0x1e280, v6
	ds_read_b32 v2, v2
	ds_read_b128 v[110:113], v206
	ds_read_b128 v[114:117], v206 offset:4096
	ds_read_b128 v[126:129], v206 offset:8192
	ds_read_b128 v[194:197], v206 offset:12288
	ds_read_b128 v[198:201], v206 offset:16384
	ds_read_b128 v[218:221], v206 offset:20480
	s_waitcnt vmcnt(20)
	ds_write_b128 v208, v[174:177] offset:24576
	s_waitcnt vmcnt(19)
	ds_write_b128 v208, v[182:185] offset:32768
	s_waitcnt vmcnt(18)
	ds_write_b128 v208, v[186:189] offset:40960
	ds_read_b128 v[174:177], v206 offset:1024
	ds_read_b128 v[182:185], v206 offset:5120
	ds_read_b128 v[186:189], v206 offset:9216
	ds_read_b128 v[222:225], v206 offset:13312
	ds_read_b128 v[226:229], v206 offset:17408
	ds_read_b128 v[230:233], v206 offset:21504
	s_waitcnt lgkmcnt(14)
	v_mov_b32_e32 v67, v66
	v_mov_b32_e32 v68, v66
	v_mov_b32_e32 v69, v66
	v_mov_b32_e32 v70, v66
	v_mov_b32_e32 v71, v66
	v_mov_b32_e32 v72, v66
	v_mov_b32_e32 v73, v66
	v_mov_b32_e32 v74, v66
	v_mov_b32_e32 v75, v66
	v_mov_b32_e32 v76, v66
	v_mov_b32_e32 v77, v66
	v_mov_b32_e32 v78, v66
	v_mov_b32_e32 v79, v66
	v_mov_b32_e32 v80, v66
	v_mov_b32_e32 v81, v66
	v_mov_b32_e32 v3, v2
	v_mov_b32_e32 v4, v2
	v_mov_b32_e32 v5, v2
	v_mov_b32_e32 v6, v2
	v_mov_b32_e32 v7, v2
	v_mov_b32_e32 v8, v2
	v_mov_b32_e32 v9, v2
	v_mov_b32_e32 v10, v2
	v_mov_b32_e32 v11, v2
	v_mov_b32_e32 v12, v2
	v_mov_b32_e32 v13, v2
	v_mov_b32_e32 v14, v2
	v_mov_b32_e32 v15, v2
	v_mov_b32_e32 v16, v2
	v_mov_b32_e32 v17, v2
	s_waitcnt vmcnt(17)
	v_mfma_f32_32x32x16_bf16 v[50:65], v[110:113], v[170:173], v[50:65]
	s_waitcnt lgkmcnt(13)
	v_mfma_f32_32x32x16_bf16 v[18:33], v[114:117], v[170:173], v[18:33]
	s_waitcnt lgkmcnt(12)
	v_mfma_f32_32x32x16_bf16 v[82:97], v[126:129], v[170:173], v[82:97]
	s_waitcnt lgkmcnt(11)
	v_mfma_f32_32x32x16_bf16 v[34:49], v[194:197], v[170:173], v[34:49]
	s_waitcnt lgkmcnt(10)
	v_mfma_f32_32x32x16_bf16 v[66:81], v[170:173], v[198:201], v[66:81]
	s_waitcnt lgkmcnt(9)
	v_mfma_f32_32x32x16_bf16 v[2:17], v[170:173], v[218:221], v[2:17]
	ds_read_b128 v[110:113], v206 offset:2048
	ds_read_b128 v[114:117], v206 offset:6144
	ds_read_b128 v[126:129], v206 offset:10240
	ds_read_b128 v[170:173], v206 offset:14336
	ds_read_b128 v[194:197], v206 offset:18432
	ds_read_b128 v[198:201], v206 offset:22528
	s_waitcnt vmcnt(16) lgkmcnt(11)
	v_mfma_f32_32x32x16_bf16 v[50:65], v[174:177], v[162:165], v[50:65]
	s_waitcnt lgkmcnt(10)
	v_mfma_f32_32x32x16_bf16 v[18:33], v[182:185], v[162:165], v[18:33]
	s_waitcnt lgkmcnt(9)
	v_mfma_f32_32x32x16_bf16 v[82:97], v[186:189], v[162:165], v[82:97]
	s_waitcnt lgkmcnt(8)
	v_mfma_f32_32x32x16_bf16 v[34:49], v[222:225], v[162:165], v[34:49]
	s_waitcnt lgkmcnt(7)
	v_mfma_f32_32x32x16_bf16 v[66:81], v[162:165], v[226:229], v[66:81]
	s_waitcnt lgkmcnt(6)
	v_mfma_f32_32x32x16_bf16 v[2:17], v[162:165], v[230:233], v[2:17]
	s_waitcnt lgkmcnt(6)
	s_barrier
	ds_read_b128 v[162:165], v206 offset:3072
	ds_read_b128 v[174:177], v206 offset:7168
	ds_read_b128 v[182:185], v206 offset:11264
	ds_read_b128 v[186:189], v206 offset:15360
	ds_read_b128 v[218:221], v206 offset:19456
	ds_read_b128 v[222:225], v206 offset:23552
	s_waitcnt vmcnt(15) lgkmcnt(11)
	v_mfma_f32_32x32x16_bf16 v[50:65], v[110:113], v[154:157], v[50:65]
	s_waitcnt lgkmcnt(10)
	v_mfma_f32_32x32x16_bf16 v[18:33], v[114:117], v[154:157], v[18:33]
	s_waitcnt lgkmcnt(9)
	v_mfma_f32_32x32x16_bf16 v[82:97], v[126:129], v[154:157], v[82:97]
	s_waitcnt lgkmcnt(8)
	v_mfma_f32_32x32x16_bf16 v[34:49], v[170:173], v[154:157], v[34:49]
	s_waitcnt lgkmcnt(7)
	v_mfma_f32_32x32x16_bf16 v[66:81], v[154:157], v[194:197], v[66:81]
	s_waitcnt lgkmcnt(6)
	v_mfma_f32_32x32x16_bf16 v[2:17], v[154:157], v[198:201], v[2:17]
	ds_read_b128 v[194:197], v206 offset:24576
	ds_read_b128 v[198:201], v206 offset:28672
	ds_read_b128 v[226:229], v206 offset:32768
	ds_read_b128 v[230:233], v206 offset:36864
	ds_read_b128 v[234:237], v206 offset:40960
	ds_read_b128 v[238:241], v206 offset:45056
	v_add_co_u32_e32 v110, vcc, s29, v204
	s_waitcnt vmcnt(14) lgkmcnt(11)
	v_mfma_f32_32x32x16_bf16 v[50:65], v[162:165], v[146:149], v[50:65]
	v_addc_co_u32_e32 v111, vcc, 0, v205, vcc
	v_add_co_u32_e32 v242, vcc, s30, v204
	s_nop 1
	v_addc_co_u32_e32 v243, vcc, 0, v205, vcc
	global_load_dwordx4 v[126:129], v[110:111], off offset:1024
	global_load_dwordx4 v[114:117], v[110:111], off offset:2048
	global_load_dwordx4 v[154:157], v[242:243], off offset:-4096
	s_nop 0
	global_load_dwordx4 v[110:113], v[110:111], off offset:3072
	s_waitcnt lgkmcnt(10)
	v_mfma_f32_32x32x16_bf16 v[18:33], v[174:177], v[146:149], v[18:33]
	s_waitcnt lgkmcnt(9)
	v_mfma_f32_32x32x16_bf16 v[82:97], v[182:185], v[146:149], v[82:97]
	s_waitcnt lgkmcnt(8)
	v_mfma_f32_32x32x16_bf16 v[34:49], v[186:189], v[146:149], v[34:49]
	s_waitcnt lgkmcnt(7)
	v_mfma_f32_32x32x16_bf16 v[66:81], v[146:149], v[218:221], v[66:81]
	s_waitcnt lgkmcnt(6)
	v_mfma_f32_32x32x16_bf16 v[2:17], v[146:149], v[222:225], v[2:17]
	v_or_b32_e32 v170, 16, v214
	v_or_b32_e32 v146, v170, v215
	v_or_b32_e32 v148, v170, v216
	v_or_b32_e32 v170, v170, v217
	v_ashrrev_i32_e32 v147, 31, v146
	v_ashrrev_i32_e32 v149, 31, v148
	v_ashrrev_i32_e32 v171, 31, v170
	v_lshlrev_b64 v[146:147], 10, v[146:147]
	v_lshlrev_b64 v[148:149], 10, v[148:149]
	v_lshlrev_b64 v[170:171], 10, v[170:171]
	v_lshl_add_u64 v[146:147], v[202:203], 0, v[146:147]
	v_lshl_add_u64 v[162:163], v[202:203], 0, v[148:149]
	v_lshl_add_u64 v[170:171], v[202:203], 0, v[170:171]
	global_load_dwordx4 v[146:149], v[146:147], off
	s_nop 0
	global_load_dwordx4 v[162:165], v[162:163], off
	v_or_b32_e32 v244, 0x10000, v206
	global_load_dwordx4 v[170:173], v[170:171], off
	v_add_u32_e32 v209, v244, v209
	s_waitcnt vmcnt(12)
	ds_write_b128 v208, v[98:101] offset:49152
	s_waitcnt vmcnt(11)
	ds_write_b128 v208, v[102:105] offset:57344
	s_waitcnt vmcnt(10)
	ds_write_b128 v209, v[106:109]
	ds_read_b128 v[98:101], v206 offset:25600
	ds_read_b128 v[102:105], v206 offset:29696
	ds_read_b128 v[106:109], v206 offset:33792
	ds_read_b128 v[174:177], v206 offset:37888
	ds_read_b128 v[182:185], v206 offset:41984
	ds_read_b128 v[186:189], v206 offset:46080
	s_waitcnt lgkmcnt(14)
	v_mfma_f32_32x32x16_bf16 v[50:65], v[194:197], v[178:181], v[50:65]
	s_waitcnt lgkmcnt(13)
	v_mfma_f32_32x32x16_bf16 v[18:33], v[198:201], v[178:181], v[18:33]
	s_waitcnt lgkmcnt(12)
	v_mfma_f32_32x32x16_bf16 v[82:97], v[226:229], v[178:181], v[82:97]
	s_waitcnt lgkmcnt(11)
	v_mfma_f32_32x32x16_bf16 v[34:49], v[230:233], v[178:181], v[34:49]
	s_waitcnt lgkmcnt(10)
	v_mfma_f32_32x32x16_bf16 v[66:81], v[178:181], v[234:237], v[66:81]
	s_waitcnt lgkmcnt(9)
	v_mfma_f32_32x32x16_bf16 v[2:17], v[178:181], v[238:241], v[2:17]
	ds_read_b128 v[178:181], v206 offset:26624
	ds_read_b128 v[194:197], v206 offset:30720
	ds_read_b128 v[198:201], v206 offset:34816
	ds_read_b128 v[218:221], v206 offset:38912
	ds_read_b128 v[222:225], v206 offset:43008
	ds_read_b128 v[226:229], v206 offset:47104
	s_waitcnt lgkmcnt(11)
	v_mfma_f32_32x32x16_bf16 v[50:65], v[98:101], v[166:169], v[50:65]
	s_waitcnt lgkmcnt(10)
	v_mfma_f32_32x32x16_bf16 v[18:33], v[102:105], v[166:169], v[18:33]
	s_waitcnt lgkmcnt(9)
	v_mfma_f32_32x32x16_bf16 v[82:97], v[106:109], v[166:169], v[82:97]
	s_waitcnt lgkmcnt(8)
	v_mfma_f32_32x32x16_bf16 v[34:49], v[174:177], v[166:169], v[34:49]
	s_waitcnt lgkmcnt(7)
	v_mfma_f32_32x32x16_bf16 v[66:81], v[166:169], v[182:185], v[66:81]
	s_waitcnt lgkmcnt(6)
	v_mfma_f32_32x32x16_bf16 v[2:17], v[166:169], v[186:189], v[2:17]
	s_waitcnt lgkmcnt(6)
	s_barrier
	ds_read_b128 v[98:101], v206 offset:27648
	ds_read_b128 v[102:105], v206 offset:31744
	ds_read_b128 v[106:109], v206 offset:35840
	ds_read_b128 v[166:169], v206 offset:39936
	ds_read_b128 v[174:177], v206 offset:44032
	ds_read_b128 v[182:185], v206 offset:48128
	s_waitcnt lgkmcnt(11)
	v_mfma_f32_32x32x16_bf16 v[50:65], v[178:181], v[158:161], v[50:65]
	s_waitcnt lgkmcnt(10)
	v_mfma_f32_32x32x16_bf16 v[18:33], v[194:197], v[158:161], v[18:33]
	s_waitcnt lgkmcnt(9)
	v_mfma_f32_32x32x16_bf16 v[82:97], v[198:201], v[158:161], v[82:97]
	s_waitcnt lgkmcnt(8)
	v_mfma_f32_32x32x16_bf16 v[34:49], v[218:221], v[158:161], v[34:49]
	s_waitcnt lgkmcnt(7)
	v_mfma_f32_32x32x16_bf16 v[66:81], v[158:161], v[222:225], v[66:81]
	s_waitcnt lgkmcnt(6)
	v_mfma_f32_32x32x16_bf16 v[2:17], v[158:161], v[226:229], v[2:17]
	ds_read_b128 v[186:189], v206 offset:49152
	ds_read_b128 v[194:197], v206 offset:53248
	ds_read_b128 v[198:201], v206 offset:57344
	ds_read_b128 v[218:221], v206 offset:61440
	v_or_b32_e32 v240, 0x11000, v206
	ds_read_b128 v[222:225], v244
	ds_read_b128 v[226:229], v240
	s_waitcnt lgkmcnt(11)
	v_mfma_f32_32x32x16_bf16 v[50:65], v[98:101], v[150:153], v[50:65]
	s_waitcnt lgkmcnt(10)
	v_mfma_f32_32x32x16_bf16 v[18:33], v[102:105], v[150:153], v[18:33]
	s_waitcnt lgkmcnt(9)
	v_mfma_f32_32x32x16_bf16 v[82:97], v[106:109], v[150:153], v[82:97]
	global_load_dwordx4 v[158:161], v[242:243], off
	global_load_dwordx4 v[106:109], v[242:243], off offset:1024
	global_load_dwordx4 v[102:105], v[242:243], off offset:2048
	global_load_dwordx4 v[98:101], v[242:243], off offset:3072
	s_waitcnt lgkmcnt(8)
	v_mfma_f32_32x32x16_bf16 v[34:49], v[166:169], v[150:153], v[34:49]
	s_waitcnt lgkmcnt(7)
	v_mfma_f32_32x32x16_bf16 v[66:81], v[150:153], v[174:177], v[66:81]
	s_waitcnt lgkmcnt(6)
	v_mfma_f32_32x32x16_bf16 v[2:17], v[150:153], v[182:185], v[2:17]
	v_or_b32_e32 v174, 20, v214
	v_or_b32_e32 v150, v174, v215
	v_or_b32_e32 v152, v174, v216
	v_or_b32_e32 v174, v174, v217
	v_ashrrev_i32_e32 v151, 31, v150
	v_ashrrev_i32_e32 v153, 31, v152
	v_ashrrev_i32_e32 v175, 31, v174
	v_lshlrev_b64 v[150:151], 10, v[150:151]
	v_lshlrev_b64 v[152:153], 10, v[152:153]
	v_lshlrev_b64 v[174:175], 10, v[174:175]
	v_lshl_add_u64 v[150:151], v[202:203], 0, v[150:151]
	v_lshl_add_u64 v[166:167], v[202:203], 0, v[152:153]
	v_lshl_add_u64 v[174:175], v[202:203], 0, v[174:175]
	global_load_dwordx4 v[150:153], v[150:151], off
	s_nop 0
	global_load_dwordx4 v[166:169], v[166:167], off
	v_or_b32_e32 v241, 0x10400, v206
	global_load_dwordx4 v[178:181], v[174:175], off
	s_waitcnt vmcnt(16)
	ds_write_b128 v208, v[118:121]
	s_waitcnt vmcnt(15)
	ds_write_b128 v208, v[122:125] offset:8192
	s_waitcnt vmcnt(14)
	ds_write_b128 v208, v[190:193] offset:16384
	ds_read_b128 v[118:121], v206 offset:50176
	ds_read_b128 v[122:125], v206 offset:54272
	ds_read_b128 v[174:177], v206 offset:58368
	ds_read_b128 v[182:185], v206 offset:62464
	v_or_b32_e32 v242, 0x11400, v206
	ds_read_b128 v[190:193], v241
	ds_read_b128 v[230:233], v242
	s_waitcnt lgkmcnt(14)
	v_mfma_f32_32x32x16_bf16 v[50:65], v[186:189], v[142:145], v[50:65]
	s_waitcnt lgkmcnt(13)
	v_mfma_f32_32x32x16_bf16 v[18:33], v[194:197], v[142:145], v[18:33]
	s_waitcnt lgkmcnt(12)
	v_mfma_f32_32x32x16_bf16 v[82:97], v[198:201], v[142:145], v[82:97]
	s_waitcnt lgkmcnt(11)
	v_mfma_f32_32x32x16_bf16 v[34:49], v[218:221], v[142:145], v[34:49]
	s_waitcnt lgkmcnt(10)
	v_mfma_f32_32x32x16_bf16 v[66:81], v[142:145], v[222:225], v[66:81]
	s_waitcnt lgkmcnt(9)
	v_mfma_f32_32x32x16_bf16 v[2:17], v[142:145], v[226:229], v[2:17]
	ds_read_b128 v[142:145], v206 offset:51200
	ds_read_b128 v[186:189], v206 offset:55296
	ds_read_b128 v[194:197], v206 offset:59392
	ds_read_b128 v[198:201], v206 offset:63488
	v_or_b32_e32 v243, 0x10800, v206
	v_or_b32_e32 v245, 0x11800, v206
	ds_read_b128 v[218:221], v243
	ds_read_b128 v[222:225], v245
	s_waitcnt lgkmcnt(11)
	v_mfma_f32_32x32x16_bf16 v[50:65], v[118:121], v[138:141], v[50:65]
	s_waitcnt lgkmcnt(10)
	v_mfma_f32_32x32x16_bf16 v[18:33], v[122:125], v[138:141], v[18:33]
	s_waitcnt lgkmcnt(9)
	v_mfma_f32_32x32x16_bf16 v[82:97], v[174:177], v[138:141], v[82:97]
	s_waitcnt lgkmcnt(8)
	v_mfma_f32_32x32x16_bf16 v[34:49], v[182:185], v[138:141], v[34:49]
	s_waitcnt lgkmcnt(7)
	v_mfma_f32_32x32x16_bf16 v[66:81], v[138:141], v[190:193], v[66:81]
	s_waitcnt lgkmcnt(6)
	v_mfma_f32_32x32x16_bf16 v[2:17], v[138:141], v[230:233], v[2:17]
	s_waitcnt lgkmcnt(6)
	s_barrier
	ds_read_b128 v[118:121], v206 offset:52224
	ds_read_b128 v[122:125], v206 offset:56320
	ds_read_b128 v[138:141], v206 offset:60416
	ds_read_b128 v[174:177], v206 offset:64512
	v_or_b32_e32 v246, 0x10c00, v206
	v_or_b32_e32 v247, 0x11c00, v206
	ds_read_b128 v[182:185], v246
	ds_read_b128 v[190:193], v247
	s_waitcnt lgkmcnt(11)
	v_mfma_f32_32x32x16_bf16 v[50:65], v[142:145], v[134:137], v[50:65]
	s_waitcnt lgkmcnt(10)
	v_mfma_f32_32x32x16_bf16 v[18:33], v[186:189], v[134:137], v[18:33]
	s_waitcnt lgkmcnt(9)
	v_mfma_f32_32x32x16_bf16 v[82:97], v[194:197], v[134:137], v[82:97]
	s_waitcnt lgkmcnt(8)
	v_mfma_f32_32x32x16_bf16 v[34:49], v[198:201], v[134:137], v[34:49]
	s_waitcnt lgkmcnt(7)
	v_mfma_f32_32x32x16_bf16 v[66:81], v[134:137], v[218:221], v[66:81]
	s_waitcnt lgkmcnt(6)
	v_mfma_f32_32x32x16_bf16 v[2:17], v[134:137], v[222:225], v[2:17]
	ds_read_b128 v[186:189], v206
	ds_read_b128 v[218:221], v206 offset:4096
	ds_read_b128 v[222:225], v206 offset:8192
	ds_read_b128 v[226:229], v206 offset:12288
	ds_read_b128 v[230:233], v206 offset:16384
	ds_read_b128 v[234:237], v206 offset:20480
	s_waitcnt lgkmcnt(11)
	v_mfma_f32_32x32x16_bf16 v[50:65], v[118:121], v[130:133], v[50:65]
	v_add_co_u32_e32 v118, vcc, s31, v204
	s_nop 1
	v_addc_co_u32_e32 v119, vcc, 0, v205, vcc
	v_add_co_u32_e32 v238, vcc, s27, v204
	s_waitcnt lgkmcnt(10)
	v_mfma_f32_32x32x16_bf16 v[18:33], v[122:125], v[130:133], v[18:33]
	v_addc_co_u32_e32 v239, vcc, 0, v205, vcc
	s_waitcnt lgkmcnt(9)
	v_mfma_f32_32x32x16_bf16 v[82:97], v[138:141], v[130:133], v[82:97]
	global_load_dwordx4 v[138:141], v[118:119], off offset:1024
	global_load_dwordx4 v[134:137], v[118:119], off offset:2048
	s_waitcnt lgkmcnt(8)
	v_mfma_f32_32x32x16_bf16 v[34:49], v[174:177], v[130:133], v[34:49]
	s_waitcnt lgkmcnt(7)
	v_mfma_f32_32x32x16_bf16 v[66:81], v[130:133], v[182:185], v[66:81]
	s_waitcnt lgkmcnt(6)
	v_mfma_f32_32x32x16_bf16 v[2:17], v[130:133], v[190:193], v[2:17]
	global_load_dwordx4 v[142:145], v[238:239], off offset:-4096
	global_load_dwordx4 v[130:133], v[118:119], off offset:3072
	v_or_b32_e32 v122, 24, v214
	v_or_b32_e32 v118, v122, v215
	v_ashrrev_i32_e32 v119, 31, v118
	v_or_b32_e32 v120, v122, v216
	v_lshlrev_b64 v[118:119], 10, v[118:119]
	v_ashrrev_i32_e32 v121, 31, v120
	v_lshl_add_u64 v[118:119], v[202:203], 0, v[118:119]
	v_lshlrev_b64 v[120:121], 10, v[120:121]
	v_lshl_add_u64 v[120:121], v[202:203], 0, v[120:121]
	global_load_dwordx4 v[190:193], v[118:119], off
	global_load_dwordx4 v[194:197], v[120:121], off
	v_or_b32_e32 v118, v122, v217
	v_ashrrev_i32_e32 v119, 31, v118
	v_lshlrev_b64 v[118:119], 10, v[118:119]
	v_lshl_add_u64 v[118:119], v[202:203], 0, v[118:119]
	global_load_dwordx4 v[198:201], v[118:119], off
	s_waitcnt vmcnt(16)
	ds_write_b128 v208, v[146:149] offset:24576
	s_waitcnt vmcnt(15)
	ds_write_b128 v208, v[162:165] offset:32768
	s_waitcnt vmcnt(14)
	ds_write_b128 v208, v[170:173] offset:40960
	ds_read_b128 v[118:121], v206 offset:1024
	ds_read_b128 v[122:125], v206 offset:5120
	ds_read_b128 v[146:149], v206 offset:9216
	ds_read_b128 v[162:165], v206 offset:13312
	ds_read_b128 v[170:173], v206 offset:17408
	ds_read_b128 v[174:177], v206 offset:21504
	s_waitcnt lgkmcnt(14)
	v_mfma_f32_32x32x16_bf16 v[50:65], v[186:189], v[154:157], v[50:65]
	s_waitcnt lgkmcnt(13)
	v_mfma_f32_32x32x16_bf16 v[18:33], v[218:221], v[154:157], v[18:33]
	s_waitcnt lgkmcnt(12)
	v_mfma_f32_32x32x16_bf16 v[82:97], v[222:225], v[154:157], v[82:97]
	s_waitcnt lgkmcnt(11)
	v_mfma_f32_32x32x16_bf16 v[34:49], v[226:229], v[154:157], v[34:49]
	s_waitcnt lgkmcnt(10)
	v_mfma_f32_32x32x16_bf16 v[66:81], v[154:157], v[230:233], v[66:81]
	s_waitcnt lgkmcnt(9)
	v_mfma_f32_32x32x16_bf16 v[2:17], v[154:157], v[234:237], v[2:17]
	ds_read_b128 v[154:157], v206 offset:2048
	ds_read_b128 v[182:185], v206 offset:6144
	ds_read_b128 v[186:189], v206 offset:10240
	ds_read_b128 v[218:221], v206 offset:14336
	ds_read_b128 v[222:225], v206 offset:18432
	ds_read_b128 v[226:229], v206 offset:22528
	s_waitcnt lgkmcnt(11)
	v_mfma_f32_32x32x16_bf16 v[50:65], v[118:121], v[126:129], v[50:65]
	s_waitcnt lgkmcnt(10)
	v_mfma_f32_32x32x16_bf16 v[18:33], v[122:125], v[126:129], v[18:33]
	s_waitcnt lgkmcnt(9)
	v_mfma_f32_32x32x16_bf16 v[82:97], v[146:149], v[126:129], v[82:97]
	s_waitcnt lgkmcnt(8)
	v_mfma_f32_32x32x16_bf16 v[34:49], v[162:165], v[126:129], v[34:49]
	s_waitcnt lgkmcnt(7)
	v_mfma_f32_32x32x16_bf16 v[66:81], v[126:129], v[170:173], v[66:81]
	s_waitcnt lgkmcnt(6)
	v_mfma_f32_32x32x16_bf16 v[2:17], v[126:129], v[174:177], v[2:17]
	s_waitcnt lgkmcnt(6)
	s_barrier
	ds_read_b128 v[118:121], v206 offset:3072
	ds_read_b128 v[122:125], v206 offset:7168
	ds_read_b128 v[126:129], v206 offset:11264
	ds_read_b128 v[146:149], v206 offset:15360
	ds_read_b128 v[162:165], v206 offset:19456
	ds_read_b128 v[174:177], v206 offset:23552
	s_waitcnt lgkmcnt(11)
	v_mfma_f32_32x32x16_bf16 v[50:65], v[154:157], v[114:117], v[50:65]
	s_waitcnt lgkmcnt(10)
	v_mfma_f32_32x32x16_bf16 v[18:33], v[182:185], v[114:117], v[18:33]
	s_waitcnt lgkmcnt(9)
	v_mfma_f32_32x32x16_bf16 v[82:97], v[186:189], v[114:117], v[82:97]
	s_waitcnt lgkmcnt(8)
	v_mfma_f32_32x32x16_bf16 v[34:49], v[218:221], v[114:117], v[34:49]
	s_waitcnt lgkmcnt(7)
	v_mfma_f32_32x32x16_bf16 v[66:81], v[114:117], v[222:225], v[66:81]
	s_waitcnt lgkmcnt(6)
	v_mfma_f32_32x32x16_bf16 v[2:17], v[114:117], v[226:229], v[2:17]
	ds_read_b128 v[114:117], v206 offset:24576
	ds_read_b128 v[218:221], v206 offset:28672
	ds_read_b128 v[222:225], v206 offset:32768
	ds_read_b128 v[226:229], v206 offset:36864
	ds_read_b128 v[230:233], v206 offset:40960
	ds_read_b128 v[234:237], v206 offset:45056
	s_waitcnt lgkmcnt(8)
	v_mfma_f32_32x32x16_bf16 v[34:49], v[146:149], v[110:113], v[34:49]
	s_waitcnt lgkmcnt(7)
	v_mfma_f32_32x32x16_bf16 v[66:81], v[110:113], v[162:165], v[66:81]
	global_load_dwordx4 v[170:173], v[238:239], off
	global_load_dwordx4 v[162:165], v[238:239], off offset:1024
	global_load_dwordx4 v[154:157], v[238:239], off offset:2048
	global_load_dwordx4 v[146:149], v[238:239], off offset:3072
	v_mfma_f32_32x32x16_bf16 v[50:65], v[118:121], v[110:113], v[50:65]
	v_mfma_f32_32x32x16_bf16 v[18:33], v[122:125], v[110:113], v[18:33]
	v_mfma_f32_32x32x16_bf16 v[82:97], v[126:129], v[110:113], v[82:97]
	s_waitcnt lgkmcnt(6)
	v_mfma_f32_32x32x16_bf16 v[2:17], v[110:113], v[174:177], v[2:17]
	v_or_b32_e32 v118, 28, v214
	v_or_b32_e32 v110, v118, v215
	v_ashrrev_i32_e32 v111, 31, v110
	v_or_b32_e32 v112, v118, v216
	v_lshlrev_b64 v[110:111], 10, v[110:111]
	v_ashrrev_i32_e32 v113, 31, v112
	v_lshl_add_u64 v[110:111], v[202:203], 0, v[110:111]
	v_lshlrev_b64 v[112:113], 10, v[112:113]
	v_lshl_add_u64 v[112:113], v[202:203], 0, v[112:113]
	global_load_dwordx4 v[174:177], v[110:111], off
	global_load_dwordx4 v[182:185], v[112:113], off
	v_or_b32_e32 v110, v118, v217
	v_ashrrev_i32_e32 v111, 31, v110
	v_lshlrev_b64 v[110:111], 10, v[110:111]
	v_lshl_add_u64 v[110:111], v[202:203], 0, v[110:111]
	global_load_dwordx4 v[186:189], v[110:111], off
	s_waitcnt vmcnt(16)
	ds_write_b128 v208, v[150:153] offset:49152
	s_waitcnt vmcnt(15)
	ds_write_b128 v208, v[166:169] offset:57344
	s_waitcnt vmcnt(14)
	ds_write_b128 v209, v[178:181]
	ds_read_b128 v[110:113], v206 offset:25600
	ds_read_b128 v[118:121], v206 offset:29696
	ds_read_b128 v[122:125], v206 offset:33792
	ds_read_b128 v[126:129], v206 offset:37888
	ds_read_b128 v[150:153], v206 offset:41984
	ds_read_b128 v[166:169], v206 offset:46080
	s_waitcnt lgkmcnt(14)
	v_mfma_f32_32x32x16_bf16 v[50:65], v[114:117], v[158:161], v[50:65]
	s_waitcnt lgkmcnt(13)
	v_mfma_f32_32x32x16_bf16 v[18:33], v[218:221], v[158:161], v[18:33]
	s_waitcnt lgkmcnt(12)
	v_mfma_f32_32x32x16_bf16 v[82:97], v[222:225], v[158:161], v[82:97]
	s_waitcnt lgkmcnt(11)
	v_mfma_f32_32x32x16_bf16 v[34:49], v[226:229], v[158:161], v[34:49]
	s_waitcnt lgkmcnt(10)
	v_mfma_f32_32x32x16_bf16 v[66:81], v[158:161], v[230:233], v[66:81]
	s_waitcnt lgkmcnt(9)
	v_mfma_f32_32x32x16_bf16 v[2:17], v[158:161], v[234:237], v[2:17]
	ds_read_b128 v[114:117], v206 offset:26624
	ds_read_b128 v[158:161], v206 offset:30720
	ds_read_b128 v[178:181], v206 offset:34816
	ds_read_b128 v[218:221], v206 offset:38912
	ds_read_b128 v[222:225], v206 offset:43008
	ds_read_b128 v[226:229], v206 offset:47104
	s_waitcnt lgkmcnt(11)
	v_mfma_f32_32x32x16_bf16 v[50:65], v[110:113], v[106:109], v[50:65]
	s_waitcnt lgkmcnt(10)
	v_mfma_f32_32x32x16_bf16 v[18:33], v[118:121], v[106:109], v[18:33]
	s_waitcnt lgkmcnt(9)
	v_mfma_f32_32x32x16_bf16 v[82:97], v[122:125], v[106:109], v[82:97]
	s_waitcnt lgkmcnt(8)
	v_mfma_f32_32x32x16_bf16 v[34:49], v[126:129], v[106:109], v[34:49]
	s_waitcnt lgkmcnt(7)
	v_mfma_f32_32x32x16_bf16 v[66:81], v[106:109], v[150:153], v[66:81]
	s_waitcnt lgkmcnt(6)
	v_mfma_f32_32x32x16_bf16 v[2:17], v[106:109], v[166:169], v[2:17]
	s_waitcnt lgkmcnt(6)
	s_barrier
	ds_read_b128 v[106:109], v206 offset:27648
	ds_read_b128 v[110:113], v206 offset:31744
	ds_read_b128 v[118:121], v206 offset:35840
	ds_read_b128 v[122:125], v206 offset:39936
	ds_read_b128 v[126:129], v206 offset:44032
	ds_read_b128 v[230:233], v206 offset:48128
	s_waitcnt lgkmcnt(11)
	v_mfma_f32_32x32x16_bf16 v[50:65], v[114:117], v[102:105], v[50:65]
	s_waitcnt lgkmcnt(10)
	v_mfma_f32_32x32x16_bf16 v[18:33], v[158:161], v[102:105], v[18:33]
	s_waitcnt lgkmcnt(9)
	v_mfma_f32_32x32x16_bf16 v[82:97], v[178:181], v[102:105], v[82:97]
	s_waitcnt lgkmcnt(8)
	v_mfma_f32_32x32x16_bf16 v[34:49], v[218:221], v[102:105], v[34:49]
	s_waitcnt lgkmcnt(7)
	v_mfma_f32_32x32x16_bf16 v[66:81], v[102:105], v[222:225], v[66:81]
	s_waitcnt lgkmcnt(6)
	v_mfma_f32_32x32x16_bf16 v[2:17], v[102:105], v[226:229], v[2:17]
	ds_read_b128 v[102:105], v206 offset:49152
	ds_read_b128 v[114:117], v206 offset:53248
	ds_read_b128 v[218:221], v206 offset:57344
	ds_read_b128 v[222:225], v206 offset:61440
	ds_read_b128 v[226:229], v244
	ds_read_b128 v[234:237], v240
	s_waitcnt lgkmcnt(11)
	v_mfma_f32_32x32x16_bf16 v[50:65], v[106:109], v[98:101], v[50:65]
	v_add_co_u32_e32 v106, vcc, s33, v204
	s_nop 1
	v_addc_co_u32_e32 v107, vcc, 0, v205, vcc
	global_load_dwordx4 v[178:181], v[106:107], off
	global_load_dwordx4 v[166:169], v[106:107], off offset:1024
	global_load_dwordx4 v[158:161], v[106:107], off offset:2048
	global_load_dwordx4 v[150:153], v[106:107], off offset:3072
	s_waitcnt lgkmcnt(10)
	v_mfma_f32_32x32x16_bf16 v[18:33], v[110:113], v[98:101], v[18:33]
	s_waitcnt lgkmcnt(9)
	v_mfma_f32_32x32x16_bf16 v[82:97], v[118:121], v[98:101], v[82:97]
	s_waitcnt lgkmcnt(8)
	v_mfma_f32_32x32x16_bf16 v[34:49], v[122:125], v[98:101], v[34:49]
	s_waitcnt lgkmcnt(7)
	v_mfma_f32_32x32x16_bf16 v[66:81], v[98:101], v[126:129], v[66:81]
	s_waitcnt lgkmcnt(6)
	v_mfma_f32_32x32x16_bf16 v[2:17], v[98:101], v[230:233], v[2:17]
	s_waitcnt vmcnt(13)
	ds_write_b128 v208, v[190:193]
	s_waitcnt vmcnt(12)
	ds_write_b128 v208, v[194:197] offset:8192
	s_waitcnt vmcnt(11)
	ds_write_b128 v208, v[198:201] offset:16384
	ds_read_b128 v[98:101], v206 offset:50176
	ds_read_b128 v[106:109], v206 offset:54272
	ds_read_b128 v[110:113], v206 offset:58368
	ds_read_b128 v[118:121], v206 offset:62464
	ds_read_b128 v[122:125], v241
	ds_read_b128 v[126:129], v242
	s_waitcnt lgkmcnt(14)
	v_mfma_f32_32x32x16_bf16 v[50:65], v[102:105], v[142:145], v[50:65]
	s_waitcnt lgkmcnt(13)
	v_mfma_f32_32x32x16_bf16 v[18:33], v[114:117], v[142:145], v[18:33]
	s_waitcnt lgkmcnt(12)
	v_mfma_f32_32x32x16_bf16 v[82:97], v[218:221], v[142:145], v[82:97]
	s_waitcnt lgkmcnt(11)
	v_mfma_f32_32x32x16_bf16 v[34:49], v[222:225], v[142:145], v[34:49]
	s_waitcnt lgkmcnt(10)
	v_mfma_f32_32x32x16_bf16 v[66:81], v[142:145], v[226:229], v[66:81]
	s_waitcnt lgkmcnt(9)
	v_mfma_f32_32x32x16_bf16 v[2:17], v[142:145], v[234:237], v[2:17]
	ds_read_b128 v[102:105], v206 offset:51200
	ds_read_b128 v[114:117], v206 offset:55296
	ds_read_b128 v[218:221], v206 offset:59392
	ds_read_b128 v[222:225], v206 offset:63488
	ds_read_b128 v[226:229], v243
	ds_read_b128 v[230:233], v245
	s_waitcnt lgkmcnt(11)
	v_mfma_f32_32x32x16_bf16 v[50:65], v[98:101], v[138:141], v[50:65]
	s_waitcnt lgkmcnt(10)
	v_mfma_f32_32x32x16_bf16 v[18:33], v[106:109], v[138:141], v[18:33]
	s_waitcnt lgkmcnt(9)
	v_mfma_f32_32x32x16_bf16 v[82:97], v[110:113], v[138:141], v[82:97]
	s_waitcnt lgkmcnt(8)
	v_mfma_f32_32x32x16_bf16 v[34:49], v[118:121], v[138:141], v[34:49]
	s_waitcnt lgkmcnt(7)
	v_mfma_f32_32x32x16_bf16 v[66:81], v[138:141], v[122:125], v[66:81]
	s_waitcnt lgkmcnt(6)
	v_mfma_f32_32x32x16_bf16 v[2:17], v[138:141], v[126:129], v[2:17]
	s_waitcnt lgkmcnt(6)
	s_barrier
	ds_read_b128 v[98:101], v206 offset:52224
	ds_read_b128 v[106:109], v206 offset:56320
	ds_read_b128 v[110:113], v206 offset:60416
	ds_read_b128 v[118:121], v206 offset:64512
	ds_read_b128 v[122:125], v246
	ds_read_b128 v[126:129], v247
	s_waitcnt lgkmcnt(11)
	v_mfma_f32_32x32x16_bf16 v[50:65], v[102:105], v[134:137], v[50:65]
	s_waitcnt lgkmcnt(10)
	v_mfma_f32_32x32x16_bf16 v[18:33], v[114:117], v[134:137], v[18:33]
	s_waitcnt lgkmcnt(9)
	v_mfma_f32_32x32x16_bf16 v[82:97], v[218:221], v[134:137], v[82:97]
	s_waitcnt lgkmcnt(8)
	v_mfma_f32_32x32x16_bf16 v[34:49], v[222:225], v[134:137], v[34:49]
	s_waitcnt lgkmcnt(7)
	v_mfma_f32_32x32x16_bf16 v[66:81], v[134:137], v[226:229], v[66:81]
	s_waitcnt lgkmcnt(6)
	v_mfma_f32_32x32x16_bf16 v[2:17], v[134:137], v[230:233], v[2:17]
	ds_read_b128 v[102:105], v206
	ds_read_b128 v[114:117], v206 offset:4096
	ds_read_b128 v[218:221], v206 offset:8192
	ds_read_b128 v[222:225], v206 offset:12288
	ds_read_b128 v[226:229], v206 offset:16384
	ds_read_b128 v[230:233], v206 offset:20480
	s_waitcnt lgkmcnt(11)
	v_mfma_f32_32x32x16_bf16 v[50:65], v[98:101], v[130:133], v[50:65]
	s_waitcnt lgkmcnt(10)
	v_mfma_f32_32x32x16_bf16 v[18:33], v[106:109], v[130:133], v[18:33]
	s_waitcnt lgkmcnt(9)
	v_mfma_f32_32x32x16_bf16 v[82:97], v[110:113], v[130:133], v[82:97]
	s_waitcnt lgkmcnt(8)
	v_mfma_f32_32x32x16_bf16 v[34:49], v[118:121], v[130:133], v[34:49]
	s_waitcnt lgkmcnt(7)
	v_mfma_f32_32x32x16_bf16 v[66:81], v[130:133], v[122:125], v[66:81]
	s_waitcnt lgkmcnt(6)
	v_mfma_f32_32x32x16_bf16 v[2:17], v[130:133], v[126:129], v[2:17]
	s_waitcnt vmcnt(6)
	ds_write_b128 v208, v[174:177] offset:24576
	s_waitcnt vmcnt(5)
	ds_write_b128 v208, v[182:185] offset:32768
	s_waitcnt vmcnt(4)
	ds_write_b128 v208, v[186:189] offset:40960
	s_lshl_b64 s[42:43], s[2:3], 9
	s_or_b64 s[42:43], s[42:43], s[6:7]
	v_or_b32_e32 v252, s42, v211
	v_mov_b32_e32 v253, s43
	v_lshlrev_b32_e32 v254, 5, v212
	v_lshlrev_b64 v[252:253], 8, v[252:253]
	v_mov_b32_e32 v255, 0
	v_lshl_add_u64 v[252:253], v[252:253], 0, v[254:255]
	v_or_b32_e32 v252, v252, v1
	v_lshl_add_u64 v[252:253], v[252:253], 2, s[8:9]
	global_load_dword v249, v[252:253], off
	global_load_dword v248, v[252:253], off offset:1024
	global_load_dword v247, v[252:253], off offset:2048
	global_load_dword v246, v[252:253], off offset:3072
	v_add_co_u32_e32 v254, vcc, s26, v252
	s_nop 1
	v_addc_co_u32_e32 v255, vcc, 0, v253, vcc
	global_load_dword v245, v[254:255], off
	global_load_dword v243, v[254:255], off offset:1024
	global_load_dword v241, v[254:255], off offset:2048
	global_load_dword v239, v[254:255], off offset:3072
	v_add_co_u32_e32 v254, vcc, s30, v252
	s_nop 1
	v_addc_co_u32_e32 v255, vcc, 0, v253, vcc
	global_load_dword v244, v[254:255], off
	global_load_dword v242, v[254:255], off offset:1024
	global_load_dword v240, v[254:255], off offset:2048
	global_load_dword v238, v[254:255], off offset:3072
	v_add_co_u32_e32 v254, vcc, s27, v252
	s_nop 1
	v_addc_co_u32_e32 v255, vcc, 0, v253, vcc
	global_load_dword v236, v[254:255], off
	global_load_dword v234, v[254:255], off offset:1024
	v_add_co_u32_e32 v254, vcc, s34, v252
	s_nop 1
	v_addc_co_u32_e32 v255, vcc, 0, v253, vcc
	global_load_dword v237, v[254:255], off
	global_load_dword v235, v[254:255], off offset:1024
	ds_read_b128 v[98:101], v206 offset:1024
	ds_read_b128 v[106:109], v206 offset:5120
	ds_read_b128 v[110:113], v206 offset:9216
	ds_read_b128 v[118:121], v206 offset:13312
	ds_read_b128 v[122:125], v206 offset:17408
	ds_read_b128 v[126:129], v206 offset:21504
	s_waitcnt lgkmcnt(14)
	v_mfma_f32_32x32x16_bf16 v[50:65], v[102:105], v[170:173], v[50:65]
	s_waitcnt lgkmcnt(13)
	v_mfma_f32_32x32x16_bf16 v[18:33], v[114:117], v[170:173], v[18:33]
	s_waitcnt lgkmcnt(12)
	v_mfma_f32_32x32x16_bf16 v[82:97], v[218:221], v[170:173], v[82:97]
	s_waitcnt lgkmcnt(11)
	v_mfma_f32_32x32x16_bf16 v[34:49], v[222:225], v[170:173], v[34:49]
	s_waitcnt lgkmcnt(10)
	v_mfma_f32_32x32x16_bf16 v[66:81], v[170:173], v[226:229], v[66:81]
	s_waitcnt lgkmcnt(9)
	v_mfma_f32_32x32x16_bf16 v[2:17], v[170:173], v[230:233], v[2:17]
	ds_read_b128 v[102:105], v206 offset:2048
	ds_read_b128 v[114:117], v206 offset:6144
	ds_read_b128 v[218:221], v206 offset:10240
	ds_read_b128 v[222:225], v206 offset:14336
	ds_read_b128 v[226:229], v206 offset:18432
	ds_read_b128 v[230:233], v206 offset:22528
	s_waitcnt lgkmcnt(11)
	v_mfma_f32_32x32x16_bf16 v[50:65], v[98:101], v[162:165], v[50:65]
	s_waitcnt lgkmcnt(10)
	v_mfma_f32_32x32x16_bf16 v[18:33], v[106:109], v[162:165], v[18:33]
	s_waitcnt lgkmcnt(9)
	v_mfma_f32_32x32x16_bf16 v[82:97], v[110:113], v[162:165], v[82:97]
	s_waitcnt lgkmcnt(8)
	v_mfma_f32_32x32x16_bf16 v[34:49], v[118:121], v[162:165], v[34:49]
	s_waitcnt lgkmcnt(7)
	v_mfma_f32_32x32x16_bf16 v[66:81], v[162:165], v[122:125], v[66:81]
	s_waitcnt lgkmcnt(6)
	v_mfma_f32_32x32x16_bf16 v[2:17], v[162:165], v[126:129], v[2:17]
	s_waitcnt lgkmcnt(6)
	s_barrier
	ds_read_b128 v[98:101], v206 offset:3072
	ds_read_b128 v[106:109], v206 offset:7168
	ds_read_b128 v[110:113], v206 offset:11264
	ds_read_b128 v[118:121], v206 offset:15360
	ds_read_b128 v[122:125], v206 offset:19456
	ds_read_b128 v[126:129], v206 offset:23552
	s_waitcnt lgkmcnt(11)
	v_mfma_f32_32x32x16_bf16 v[50:65], v[102:105], v[154:157], v[50:65]
	s_waitcnt lgkmcnt(10)
	v_mfma_f32_32x32x16_bf16 v[18:33], v[114:117], v[154:157], v[18:33]
	s_waitcnt lgkmcnt(9)
	v_mfma_f32_32x32x16_bf16 v[82:97], v[218:221], v[154:157], v[82:97]
	s_waitcnt lgkmcnt(8)
	v_mfma_f32_32x32x16_bf16 v[34:49], v[222:225], v[154:157], v[34:49]
	s_waitcnt lgkmcnt(7)
	v_mfma_f32_32x32x16_bf16 v[66:81], v[154:157], v[226:229], v[66:81]
	s_waitcnt lgkmcnt(6)
	v_mfma_f32_32x32x16_bf16 v[2:17], v[154:157], v[230:233], v[2:17]
	ds_read_b128 v[102:105], v206 offset:24576
	ds_read_b128 v[114:117], v206 offset:28672
	ds_read_b128 v[218:221], v206 offset:32768
	ds_read_b128 v[222:225], v206 offset:36864
	ds_read_b128 v[226:229], v206 offset:40960
	ds_read_b128 v[230:233], v206 offset:45056
	s_waitcnt lgkmcnt(11)
	v_mfma_f32_32x32x16_bf16 v[50:65], v[98:101], v[146:149], v[50:65]
	s_waitcnt lgkmcnt(10)
	v_mfma_f32_32x32x16_bf16 v[18:33], v[106:109], v[146:149], v[18:33]
	s_waitcnt lgkmcnt(9)
	v_mfma_f32_32x32x16_bf16 v[82:97], v[110:113], v[146:149], v[82:97]
	s_waitcnt lgkmcnt(8)
	v_mfma_f32_32x32x16_bf16 v[34:49], v[118:121], v[146:149], v[34:49]
	s_waitcnt lgkmcnt(7)
	v_mfma_f32_32x32x16_bf16 v[66:81], v[146:149], v[122:125], v[66:81]
	s_waitcnt lgkmcnt(6)
	v_mfma_f32_32x32x16_bf16 v[2:17], v[146:149], v[126:129], v[2:17]
	ds_read_b128 v[98:101], v206 offset:25600
	ds_read_b128 v[106:109], v206 offset:29696
	ds_read_b128 v[110:113], v206 offset:33792
	ds_read_b128 v[118:121], v206 offset:37888
	ds_read_b128 v[122:125], v206 offset:41984
	ds_read_b128 v[126:129], v206 offset:46080
	s_waitcnt vmcnt(19) lgkmcnt(11)
	v_mfma_f32_32x32x16_bf16 v[50:65], v[102:105], v[178:181], v[50:65]
	s_waitcnt lgkmcnt(10)
	v_mfma_f32_32x32x16_bf16 v[18:33], v[114:117], v[178:181], v[18:33]
	s_waitcnt lgkmcnt(9)
	v_mfma_f32_32x32x16_bf16 v[82:97], v[218:221], v[178:181], v[82:97]
	s_waitcnt lgkmcnt(8)
	v_mfma_f32_32x32x16_bf16 v[34:49], v[222:225], v[178:181], v[34:49]
	s_waitcnt lgkmcnt(7)
	v_mfma_f32_32x32x16_bf16 v[66:81], v[178:181], v[226:229], v[66:81]
	s_waitcnt lgkmcnt(6)
	v_mfma_f32_32x32x16_bf16 v[2:17], v[178:181], v[230:233], v[2:17]
	ds_read_b128 v[102:105], v206 offset:26624
	ds_read_b128 v[114:117], v206 offset:30720
	ds_read_b128 v[218:221], v206 offset:34816
	ds_read_b128 v[222:225], v206 offset:38912
	ds_read_b128 v[226:229], v206 offset:43008
	ds_read_b128 v[230:233], v206 offset:47104
	s_waitcnt vmcnt(18) lgkmcnt(11)
	v_mfma_f32_32x32x16_bf16 v[50:65], v[98:101], v[166:169], v[50:65]
	s_waitcnt lgkmcnt(10)
	v_mfma_f32_32x32x16_bf16 v[18:33], v[106:109], v[166:169], v[18:33]
	s_waitcnt lgkmcnt(9)
	v_mfma_f32_32x32x16_bf16 v[82:97], v[110:113], v[166:169], v[82:97]
	s_waitcnt lgkmcnt(8)
	v_mfma_f32_32x32x16_bf16 v[34:49], v[118:121], v[166:169], v[34:49]
	s_waitcnt lgkmcnt(7)
	v_mfma_f32_32x32x16_bf16 v[66:81], v[166:169], v[122:125], v[66:81]
	s_waitcnt lgkmcnt(6)
	v_mfma_f32_32x32x16_bf16 v[2:17], v[166:169], v[126:129], v[2:17]
	s_waitcnt lgkmcnt(6)
	s_barrier
	ds_read_b128 v[98:101], v206 offset:27648
	ds_read_b128 v[106:109], v206 offset:31744
	ds_read_b128 v[110:113], v206 offset:35840
	ds_read_b128 v[118:121], v206 offset:39936
	ds_read_b128 v[122:125], v206 offset:44032
	ds_read_b128 v[126:129], v206 offset:48128
	s_waitcnt vmcnt(17) lgkmcnt(11)
	v_mfma_f32_32x32x16_bf16 v[50:65], v[102:105], v[158:161], v[50:65]
	s_waitcnt lgkmcnt(10)
	v_mfma_f32_32x32x16_bf16 v[18:33], v[114:117], v[158:161], v[18:33]
	s_waitcnt lgkmcnt(9)
	v_mfma_f32_32x32x16_bf16 v[82:97], v[218:221], v[158:161], v[82:97]
	s_waitcnt lgkmcnt(8)
	v_mfma_f32_32x32x16_bf16 v[34:49], v[222:225], v[158:161], v[34:49]
	s_waitcnt lgkmcnt(7)
	v_mfma_f32_32x32x16_bf16 v[66:81], v[158:161], v[226:229], v[66:81]
	s_waitcnt lgkmcnt(6)
	v_mfma_f32_32x32x16_bf16 v[2:17], v[158:161], v[230:233], v[2:17]
	v_add_co_u32_e32 v254, vcc, s27, v252
	s_nop 1
	v_addc_co_u32_e32 v255, vcc, 0, v253, vcc
	global_load_dword v232, v[254:255], off offset:2048
	global_load_dword v230, v[254:255], off offset:3072
	v_add_co_u32_e32 v254, vcc, s34, v252
	s_nop 1
	v_addc_co_u32_e32 v255, vcc, 0, v253, vcc
	global_load_dword v233, v[254:255], off offset:2048
	global_load_dword v231, v[254:255], off offset:3072
	v_add_co_u32_e32 v254, vcc, s35, v252
	s_nop 1
	v_addc_co_u32_e32 v255, vcc, 0, v253, vcc
	global_load_dword v228, v[254:255], off
	global_load_dword v226, v[254:255], off offset:1024
	global_load_dword v224, v[254:255], off offset:2048
	global_load_dword v222, v[254:255], off offset:3072
	v_add_co_u32_e32 v254, vcc, s36, v252
	s_nop 1
	v_addc_co_u32_e32 v255, vcc, 0, v253, vcc
	global_load_dword v229, v[254:255], off
	global_load_dword v227, v[254:255], off offset:1024
	global_load_dword v225, v[254:255], off offset:2048
	global_load_dword v223, v[254:255], off offset:3072
	v_add_co_u32_e32 v254, vcc, s37, v252
	s_nop 1
	v_addc_co_u32_e32 v255, vcc, 0, v253, vcc
	global_load_dword v221, v[254:255], off
	global_load_dword v220, v[254:255], off offset:1024
	global_load_dword v219, v[254:255], off offset:2048
	global_load_dword v218, v[254:255], off offset:3072
	s_waitcnt vmcnt(32) lgkmcnt(5)
	v_mfma_f32_32x32x16_bf16 v[50:65], v[98:101], v[150:153], v[50:65]
	s_waitcnt lgkmcnt(4)
	v_mfma_f32_32x32x16_bf16 v[18:33], v[106:109], v[150:153], v[18:33]
	s_waitcnt lgkmcnt(3)
	v_mfma_f32_32x32x16_bf16 v[82:97], v[110:113], v[150:153], v[82:97]
	s_waitcnt lgkmcnt(2)
	v_mfma_f32_32x32x16_bf16 v[34:49], v[118:121], v[150:153], v[34:49]
	s_waitcnt lgkmcnt(1)
	v_mfma_f32_32x32x16_bf16 v[66:81], v[150:153], v[122:125], v[66:81]
	s_waitcnt lgkmcnt(0)
	v_mfma_f32_32x32x16_bf16 v[2:17], v[150:153], v[126:129], v[2:17]
	s_lshl_b64 s[42:43], s[2:3], 9
	s_or_b64 s[42:43], s[42:43], s[6:7]
	v_or_b32_e32 v98, s42, v211
	v_mov_b32_e32 v99, s43
	v_lshlrev_b32_e32 v100, 5, v212
	v_lshlrev_b64 v[98:99], 8, v[98:99]
	v_ashrrev_i32_e32 v101, 31, v100
	v_lshl_add_u64 v[208:209], v[98:99], 0, v[100:101]
	v_or_b32_e32 v208, v208, v1
	s_barrier
	s_and_b64 vcc, exec, s[18:19]
	s_cbranch_vccnz .LBB3_141
	v_or_b32_e32 v100, v215, v214
	v_ashrrev_i32_e32 v101, 31, v100
	v_or_b32_e32 v102, v216, v214
	v_lshlrev_b64 v[100:101], 10, v[100:101]
	v_ashrrev_i32_e32 v103, 31, v102
	v_lshl_add_u64 v[100:101], v[202:203], 0, v[100:101]
	v_lshlrev_b64 v[102:103], 10, v[102:103]
	v_lshl_add_u64 v[102:103], v[202:203], 0, v[102:103]
	global_load_dwordx4 v[190:193], v[100:101], off
	global_load_dwordx4 v[194:197], v[102:103], off
	v_or_b32_e32 v100, v217, v214
	v_or_b32_e32 v104, 4, v214
	v_ashrrev_i32_e32 v101, 31, v100
	v_or_b32_e32 v102, v104, v215
	v_lshlrev_b64 v[100:101], 10, v[100:101]
	v_ashrrev_i32_e32 v103, 31, v102
	v_add_u32_e32 v98, s28, v212
	v_lshl_add_u64 v[100:101], v[202:203], 0, v[100:101]
	v_lshlrev_b64 v[102:103], 10, v[102:103]
	v_ashrrev_i32_e32 v99, 31, v98
	v_lshl_add_u64 v[102:103], v[202:203], 0, v[102:103]
	global_load_dwordx4 v[198:201], v[100:101], off
	global_load_dwordx4 v[174:177], v[102:103], off
	v_or_b32_e32 v100, v216, v104
	v_lshlrev_b64 v[98:99], 15, v[98:99]
	v_ashrrev_i32_e32 v101, 31, v100
	v_or_b32_e32 v102, v217, v104
	v_lshl_add_u64 v[98:99], s[10:11], 0, v[98:99]
	v_lshlrev_b64 v[100:101], 10, v[100:101]
	v_ashrrev_i32_e32 v103, 31, v102
	v_lshl_add_u64 v[98:99], v[98:99], 0, v[206:207]
	v_lshl_add_u64 v[100:101], v[202:203], 0, v[100:101]
	v_lshlrev_b64 v[102:103], 10, v[102:103]
	v_lshl_add_u64 v[102:103], v[202:203], 0, v[102:103]
	global_load_dwordx4 v[182:185], v[100:101], off
	global_load_dwordx4 v[186:189], v[102:103], off
	global_load_dwordx4 v[170:173], v[98:99], off
	global_load_dwordx4 v[162:165], v[98:99], off offset:1024
	global_load_dwordx4 v[154:157], v[98:99], off offset:2048
	global_load_dwordx4 v[146:149], v[98:99], off offset:3072
	v_add_co_u32_e32 v100, vcc, 0x1000, v98
	s_nop 1
	v_addc_co_u32_e32 v101, vcc, 0, v99, vcc
	v_add_co_u32_e32 v98, vcc, 0x2000, v98
	global_load_dwordx4 v[178:181], v[100:101], off
	global_load_dwordx4 v[166:169], v[100:101], off offset:1024
	global_load_dwordx4 v[158:161], v[100:101], off offset:2048
	global_load_dwordx4 v[150:153], v[100:101], off offset:3072
	v_addc_co_u32_e32 v99, vcc, 0, v99, vcc
	global_load_dwordx4 v[142:145], v[98:99], off
	global_load_dwordx4 v[138:141], v[98:99], off offset:1024
	global_load_dwordx4 v[134:137], v[98:99], off offset:2048
	global_load_dwordx4 v[130:133], v[98:99], off offset:3072
	s_branch .LBB3_141

	.amdhsa_kernel _Z12fused_kernelPKDv4_jS1_S1_PKfS3_S3_PfS4_
		.amdhsa_group_segment_fixed_size 124928
		.amdhsa_private_segment_fixed_size 0
		.amdhsa_kernarg_size 64
		.amdhsa_user_sgpr_count 2
		.amdhsa_user_sgpr_dispatch_ptr 0
		.amdhsa_user_sgpr_queue_ptr 0
		.amdhsa_user_sgpr_kernarg_segment_ptr 1
		.amdhsa_user_sgpr_dispatch_id 0
		.amdhsa_user_sgpr_kernarg_preload_length 0
		.amdhsa_user_sgpr_kernarg_preload_offset 0
		.amdhsa_user_sgpr_private_segment_size 0
		.amdhsa_uses_dynamic_stack 0
		.amdhsa_enable_private_segment 0
		.amdhsa_system_sgpr_workgroup_id_x 1
		.amdhsa_system_sgpr_workgroup_id_y 0
		.amdhsa_system_sgpr_workgroup_id_z 0
		.amdhsa_system_sgpr_workgroup_info 0
		.amdhsa_system_vgpr_workitem_id 0
		.amdhsa_next_free_vgpr 256
		.amdhsa_next_free_sgpr 96
		.amdhsa_accum_offset 256
		.amdhsa_reserve_vcc 1
		.amdhsa_float_round_mode_32 0
		.amdhsa_float_round_mode_16_64 0
		.amdhsa_float_denorm_mode_32 3
		.amdhsa_float_denorm_mode_16_64 3
		.amdhsa_dx10_clamp 1
		.amdhsa_ieee_mode 1
		.amdhsa_fp16_overflow 0
		.amdhsa_tg_split 0
		.amdhsa_exception_fp_ieee_invalid_op 0
		.amdhsa_exception_fp_denorm_src 0
		.amdhsa_exception_fp_ieee_div_zero 0
		.amdhsa_exception_fp_ieee_overflow 0
		.amdhsa_exception_fp_ieee_underflow 0
		.amdhsa_exception_fp_ieee_inexact 0
		.amdhsa_exception_int_div_zero 0
	.end_amdhsa_kernel

amdhsa.kernels:
  - .agpr_count:     0
    .args:
      - .actual_access:  read_only
        .address_space:  global
        .offset:         0
        .size:           8
        .value_kind:     global_buffer
      - .actual_access:  read_only
        .address_space:  global
        .offset:         8
        .size:           8
        .value_kind:     global_buffer
      - .actual_access:  write_only
        .address_space:  global
        .offset:         16
        .size:           8
        .value_kind:     global_buffer
      - .actual_access:  write_only
        .address_space:  global
        .offset:         24
        .size:           8
        .value_kind:     global_buffer
      - .actual_access:  write_only
        .address_space:  global
        .offset:         32
        .size:           8
        .value_kind:     global_buffer
    .group_segment_fixed_size: 32896
    .kernarg_segment_align: 8
    .kernarg_segment_size: 40
    .language:       OpenCL C
    .language_version:
      - 2
      - 0
    .max_flat_workgroup_size: 256
    .name:           _Z11prep_kernelPKfS0_PDv4_jS2_Pf
    .private_segment_fixed_size: 0
    .sgpr_count:     19
    .sgpr_spill_count: 0
    .symbol:         _Z11prep_kernelPKfS0_PDv4_jS2_Pf.kd
    .uniform_work_group_size: 1
    .uses_dynamic_stack: false
    .vgpr_count:     115
    .vgpr_spill_count: 0
    .wavefront_size: 64
  - .agpr_count:     0
    .args:
      - .actual_access:  read_only
        .address_space:  global
        .offset:         0
        .size:           8
        .value_kind:     global_buffer
      - .actual_access:  read_only
        .address_space:  global
        .offset:         8
        .size:           8
        .value_kind:     global_buffer
      - .actual_access:  read_only
        .address_space:  global
        .offset:         16
        .size:           8
        .value_kind:     global_buffer
      - .actual_access:  read_only
        .address_space:  global
        .offset:         24
        .size:           8
        .value_kind:     global_buffer
      - .actual_access:  read_only
        .address_space:  global
        .offset:         32
        .size:           8
        .value_kind:     global_buffer
      - .actual_access:  read_only
        .address_space:  global
        .offset:         40
        .size:           8
        .value_kind:     global_buffer
      - .actual_access:  read_only
        .address_space:  global
        .offset:         48
        .size:           8
        .value_kind:     global_buffer
      - .actual_access:  read_only
        .address_space:  global
        .offset:         56
        .size:           8
        .value_kind:     global_buffer
      - .actual_access:  read_only
        .address_space:  global
        .offset:         64
        .size:           8
        .value_kind:     global_buffer
      - .actual_access:  write_only
        .address_space:  global
        .offset:         72
        .size:           8
        .value_kind:     global_buffer
      - .actual_access:  write_only
        .address_space:  global
        .offset:         80
        .size:           8
        .value_kind:     global_buffer
    .group_segment_fixed_size: 6400
    .kernarg_segment_align: 8
    .kernarg_segment_size: 88
    .language:       OpenCL C
    .language_version:
      - 2
      - 0
    .max_flat_workgroup_size: 256
    .name:           _Z11fold_kernelPKfS0_S0_S0_S0_S0_S0_S0_S0_PDv4_jPf
    .private_segment_fixed_size: 0
    .sgpr_count:     30
    .sgpr_spill_count: 0
    .symbol:         _Z11fold_kernelPKfS0_S0_S0_S0_S0_S0_S0_S0_PDv4_jPf.kd
    .uniform_work_group_size: 1
    .uses_dynamic_stack: false
    .vgpr_count:     72
    .vgpr_spill_count: 0
    .wavefront_size: 64
  - .agpr_count:     0
    .args:
      - .actual_access:  read_only
        .address_space:  global
        .offset:         0
        .size:           8
        .value_kind:     global_buffer
      - .actual_access:  read_only
        .address_space:  global
        .offset:         8
        .size:           8
        .value_kind:     global_buffer
      - .actual_access:  read_only
        .address_space:  global
        .offset:         16
        .size:           8
        .value_kind:     global_buffer
      - .actual_access:  write_only
        .address_space:  global
        .offset:         24
        .size:           8
        .value_kind:     global_buffer
    .group_segment_fixed_size: 37888
    .kernarg_segment_align: 8
    .kernarg_segment_size: 32
    .language:       OpenCL C
    .language_version:
      - 2
      - 0
    .max_flat_workgroup_size: 512
    .name:           _Z17audio_proj_kernelPKDv4_jS1_PKfPS_
    .private_segment_fixed_size: 0
    .sgpr_count:     22
    .sgpr_spill_count: 0
    .symbol:         _Z17audio_proj_kernelPKDv4_jS1_PKfPS_.kd
    .uniform_work_group_size: 1
    .uses_dynamic_stack: false
    .vgpr_count:     150
    .vgpr_spill_count: 0
    .wavefront_size: 64
  - .agpr_count:     0
    .args:
      - .actual_access:  read_only
        .address_space:  global
        .offset:         0
        .size:           8
        .value_kind:     global_buffer
      - .actual_access:  read_only
        .address_space:  global
        .offset:         8
        .size:           8
        .value_kind:     global_buffer
      - .actual_access:  read_only
        .address_space:  global
        .offset:         16
        .size:           8
        .value_kind:     global_buffer
      - .actual_access:  read_only
        .address_space:  global
        .offset:         24
        .size:           8
        .value_kind:     global_buffer
      - .actual_access:  read_only
        .address_space:  global
        .offset:         32
        .size:           8
        .value_kind:     global_buffer
      - .actual_access:  read_only
        .address_space:  global
        .offset:         40
        .size:           8
        .value_kind:     global_buffer
      - .actual_access:  write_only
        .address_space:  global
        .offset:         48
        .size:           8
        .value_kind:     global_buffer
      - .actual_access:  write_only
        .address_space:  global
        .offset:         56
        .size:           8
        .value_kind:     global_buffer
    .group_segment_fixed_size: 124928
    .kernarg_segment_align: 8
    .kernarg_segment_size: 64
    .language:       OpenCL C
    .language_version:
      - 2
      - 0
    .max_flat_workgroup_size: 512
    .name:           _Z12fused_kernelPKDv4_jS1_S1_PKfS3_S3_PfS4_
    .private_segment_fixed_size: 0
    .sgpr_count:     50
    .sgpr_spill_count: 0
    .symbol:         _Z12fused_kernelPKDv4_jS1_S1_PKfS3_S3_PfS4_.kd
    .uniform_work_group_size: 1
    .uses_dynamic_stack: false
    .vgpr_count:     256
    .vgpr_spill_count: 0
    .wavefront_size: 64
